# baseline (speedup 1.0000x reference)
_Z5k_fftPKtPtPKDv2_f:
	s_load_dwordx2 s[6:7], s[0:1], 0x10
	s_load_dwordx2 s[8:9], s[0:1], 0x0
	v_and_b32_e32 v1, 0xf0, v0
	v_and_b32_e32 v18, 15, v0
	v_mul_u32_u24_e32 v1, v1, v18
	v_lshlrev_b32_e32 v1, 3, v1
	s_waitcnt lgkmcnt(0)
	global_load_dwordx2 v[86:87], v1, s[6:7]
	s_lshr_b32 s4, s2, 3
	s_and_b32 s3, s2, 7
	s_and_b32 s4, s4, 0x1ffffff8
	s_or_b32 s4, s4, s3
	s_bfe_u32 s16, s2, 0x30003
	s_lshl_b32 s3, s4, 3
	s_or_b32 s3, s3, s16
	s_mov_b32 s11, 0
	s_lshr_b32 s10, s3, 1
	s_lshl_b64 s[10:11], s[10:11], 14
	s_add_u32 s3, s8, s10
	s_addc_u32 s8, s9, s11
	s_lshr_b32 s2, s2, 2
	s_and_b32 s2, s2, 2
	s_add_u32 s2, s3, s2
	v_mov_b32_e32 v3, 0
	v_lshlrev_b32_e32 v2, 2, v0
	s_addc_u32 s3, s8, 0
	s_movk_i32 s5, 0x1000
	v_lshl_add_u64 v[6:7], s[2:3], 0, v[2:3]
	v_add_co_u32_e32 v8, vcc, s5, v6
	s_movk_i32 s12, 0x2000
	s_nop 0
	v_addc_co_u32_e32 v9, vcc, 0, v7, vcc
	v_add_co_u32_e32 v10, vcc, s12, v6
	s_movk_i32 s13, 0x3000
	s_add_u32 s8, s2, 0x1000000
	v_addc_co_u32_e32 v11, vcc, 0, v7, vcc
	s_addc_u32 s9, s3, 0
	s_add_u32 s20, s2, 0x2000000
	s_addc_u32 s21, s3, 0
	v_add_co_u32_e32 v6, vcc, s13, v6
	v_lshl_add_u64 v[12:13], s[8:9], 0, v[2:3]
	s_nop 0
	v_addc_co_u32_e32 v7, vcc, 0, v7, vcc
	v_add_co_u32_e32 v14, vcc, s5, v12
	v_lshlrev_b32_e32 v1, 3, v0
	s_nop 0
	v_addc_co_u32_e32 v15, vcc, 0, v13, vcc
	v_add_co_u32_e32 v16, vcc, s12, v12
	v_or_b32_e32 v19, 0x1000, v2
	s_nop 0
	v_addc_co_u32_e32 v17, vcc, 0, v13, vcc
	v_add_co_u32_e32 v12, vcc, s13, v12
	v_or_b32_e32 v20, 0x2000, v2
	v_or_b32_e32 v21, 0x3000, v2
	v_addc_co_u32_e32 v13, vcc, 0, v13, vcc
	v_mul_u32_u24_e32 v3, 3, v0
	s_movk_i32 s5, 0x888
	v_lshlrev_b32_e32 v3, 3, v3
	s_mov_b32 s10, 0x3ec3ef15
	s_mov_b32 s11, 0xbf6c835e
	s_mov_b32 s14, s11
	s_mov_b32 s15, s10
	s_mov_b32 s12, 0xbf3504f3
	s_mov_b32 s13, s12
	v_mov_b32_e32 v88, v0
	global_load_ushort v32, v2, s[2:3] nt
	global_load_ushort v33, v2, s[8:9] nt
	global_load_ushort v34, v2, s[2:3] offset:1024 nt
	global_load_ushort v35, v2, s[8:9] offset:1024 nt
	global_load_ushort v36, v2, s[2:3] offset:2048 nt
	global_load_ushort v37, v2, s[8:9] offset:2048 nt
	global_load_ushort v38, v2, s[8:9] offset:3072 nt
	global_load_ushort v39, v2, s[2:3] offset:3072 nt
	global_load_ushort v40, v19, s[2:3] nt
	global_load_ushort v41, v19, s[8:9] nt
	global_load_ushort v42, v[8:9], off offset:1024 nt
	global_load_ushort v43, v[14:15], off offset:1024 nt
	global_load_ushort v44, v[8:9], off offset:2048 nt
	global_load_ushort v45, v[14:15], off offset:2048 nt
	global_load_ushort v46, v[14:15], off offset:3072 nt
	global_load_ushort v47, v[8:9], off offset:3072 nt
	global_load_ushort v48, v20, s[2:3] nt
	global_load_ushort v49, v20, s[8:9] nt
	global_load_ushort v50, v[10:11], off offset:1024 nt
	global_load_ushort v51, v[16:17], off offset:1024 nt
	global_load_ushort v52, v[10:11], off offset:2048 nt
	global_load_ushort v53, v[16:17], off offset:2048 nt
	global_load_ushort v54, v[16:17], off offset:3072 nt
	global_load_ushort v55, v[10:11], off offset:3072 nt
	global_load_ushort v56, v21, s[2:3] nt
	global_load_ushort v57, v21, s[8:9] nt
	global_load_ushort v58, v[6:7], off offset:1024 nt
	global_load_ushort v59, v[12:13], off offset:1024 nt
	global_load_ushort v60, v[6:7], off offset:2048 nt
	global_load_ushort v61, v[12:13], off offset:2048 nt
	global_load_ushort v62, v[12:13], off offset:3072 nt
	global_load_ushort v63, v[6:7], off offset:3072 nt
	v_mul_u32_u24_e32 v5, 5, v0
	v_mul_u32_u24_e32 v6, 6, v0
	v_mul_u32_u24_e32 v7, 7, v0
	v_mul_u32_u24_e32 v9, 9, v0
	v_mul_u32_u24_e32 v10, 10, v0
	v_lshrrev_b32_e32 v16, 1, v0
	v_lshlrev_b32_e32 v2, 4, v0
	v_lshlrev_b32_e32 v4, 5, v0
	v_lshlrev_b32_e32 v8, 6, v0
	v_mul_u32_u24_e32 v11, 11, v0
	v_mul_u32_u24_e32 v12, 12, v0
	v_mul_u32_u24_e32 v13, 13, v0
	v_mul_u32_u24_e32 v14, 14, v0
	v_mul_u32_u24_e32 v15, 15, v0
	v_lshlrev_b32_e32 v5, 3, v5
	v_lshlrev_b32_e32 v6, 3, v6
	v_lshlrev_b32_e32 v7, 3, v7
	v_lshlrev_b32_e32 v9, 3, v9
	v_lshlrev_b32_e32 v64, 3, v10
	v_and_b32_e32 v10, 0x78, v16
	v_lshlrev_b32_e32 v65, 3, v11
	v_lshlrev_b32_e32 v66, 3, v12
	v_lshlrev_b32_e32 v67, 3, v13
	v_lshlrev_b32_e32 v68, 3, v14
	v_lshlrev_b32_e32 v69, 3, v15
	v_mad_u32_u24 v96, v18, s5, v10
	global_load_dwordx2 v[30:31], v1, s[6:7]
	global_load_dwordx2 v[28:29], v2, s[6:7]
	global_load_dwordx2 v[24:25], v4, s[6:7]
	global_load_dwordx2 v[22:23], v8, s[6:7]
	s_nop 0
	s_mov_b32 s6, 0x3f6c835e
	s_mov_b32 s7, 0xbec3ef15
	s_mov_b32 s8, 0x3f3504f3
	s_mov_b32 s9, s8
	s_waitcnt vmcnt(34)
	v_lshl_or_b32 v85, v33, 16, v32
	v_cvt_f32_fp8_e32 v32, v85
	s_waitcnt vmcnt(32)
	v_lshl_or_b32 v84, v35, 16, v34
	v_cvt_f32_fp8_sdwa v33, v85 src0_sel:BYTE_2
	s_waitcnt vmcnt(30)
	v_lshl_or_b32 v83, v37, 16, v36
	v_cvt_f32_fp8_e32 v34, v84
	v_cvt_f32_fp8_sdwa v35, v84 src0_sel:BYTE_2
	s_waitcnt vmcnt(28)
	v_lshl_or_b32 v82, v38, 16, v39
	s_waitcnt vmcnt(26)
	v_lshl_or_b32 v81, v41, 16, v40
	v_cvt_f32_fp8_e32 v40, v81
	s_waitcnt vmcnt(24)
	v_lshl_or_b32 v80, v43, 16, v42
	v_cvt_f32_fp8_sdwa v41, v81 src0_sel:BYTE_2
	s_waitcnt vmcnt(22)
	v_lshl_or_b32 v79, v45, 16, v44
	v_cvt_f32_fp8_e32 v42, v80
	v_cvt_f32_fp8_sdwa v43, v80 src0_sel:BYTE_2
	v_cvt_f32_fp8_e32 v36, v83
	v_cvt_f32_fp8_sdwa v37, v83 src0_sel:BYTE_2
	s_waitcnt vmcnt(20)
	v_lshl_or_b32 v78, v46, 16, v47
	v_cvt_f32_fp8_e32 v44, v79
	s_waitcnt vmcnt(18)
	v_lshl_or_b32 v77, v49, 16, v48
	v_cvt_f32_fp8_e32 v48, v77
	s_waitcnt vmcnt(16)
	v_lshl_or_b32 v76, v51, 16, v50
	v_cvt_f32_fp8_sdwa v49, v77 src0_sel:BYTE_2
	s_waitcnt vmcnt(14)
	v_lshl_or_b32 v75, v53, 16, v52
	v_cvt_f32_fp8_e32 v50, v76
	v_cvt_f32_fp8_sdwa v51, v76 src0_sel:BYTE_2
	s_waitcnt vmcnt(12)
	v_lshl_or_b32 v74, v54, 16, v55
	s_waitcnt vmcnt(10)
	v_lshl_or_b32 v73, v57, 16, v56
	v_cvt_f32_fp8_e32 v56, v73
	s_waitcnt vmcnt(8)
	v_lshl_or_b32 v72, v59, 16, v58
	v_cvt_f32_fp8_sdwa v57, v73 src0_sel:BYTE_2
	s_waitcnt vmcnt(6)
	v_lshl_or_b32 v71, v61, 16, v60
	v_cvt_f32_fp8_e32 v58, v72
	v_cvt_f32_fp8_sdwa v59, v72 src0_sel:BYTE_2
	v_cvt_f32_fp8_sdwa v45, v79 src0_sel:BYTE_2
	v_cvt_f32_fp8_e32 v52, v75
	v_cvt_f32_fp8_sdwa v53, v75 src0_sel:BYTE_2
	v_cvt_f32_fp8_e32 v60, v71
	v_cvt_f32_fp8_sdwa v61, v71 src0_sel:BYTE_2
	s_waitcnt vmcnt(4)
	v_lshl_or_b32 v70, v62, 16, v63
	v_cvt_f32_fp8_e32 v38, v82
	v_cvt_f32_fp8_sdwa v39, v82 src0_sel:BYTE_2
	v_cvt_f32_fp8_e32 v46, v78
	v_cvt_f32_fp8_sdwa v47, v78 src0_sel:BYTE_2
	v_cvt_f32_fp8_e32 v54, v74
	v_cvt_f32_fp8_sdwa v55, v74 src0_sel:BYTE_2
	v_cvt_f32_fp8_e32 v62, v70
	v_cvt_f32_fp8_sdwa v63, v70 src0_sel:BYTE_2
	v_pk_add_f32 v[64:65], v[32:33], v[48:49]
	v_pk_add_f32 v[32:33], v[32:33], v[48:49] neg_lo:[0,1] neg_hi:[0,1]
	v_pk_add_f32 v[48:49], v[40:41], v[56:57]
	v_pk_add_f32 v[40:41], v[40:41], v[56:57] neg_lo:[0,1] neg_hi:[0,1]
	v_pk_add_f32 v[56:57], v[64:65], v[48:49]
	v_pk_add_f32 v[48:49], v[64:65], v[48:49] neg_lo:[0,1] neg_hi:[0,1]
	v_pk_add_f32 v[64:65], v[32:33], v[40:41] op_sel:[0,1] op_sel_hi:[1,0] neg_hi:[0,1]
	v_pk_add_f32 v[32:33], v[32:33], v[40:41] op_sel:[0,1] op_sel_hi:[1,0] neg_lo:[0,1]
	v_pk_add_f32 v[40:41], v[34:35], v[50:51]
	v_pk_add_f32 v[34:35], v[34:35], v[50:51] neg_lo:[0,1] neg_hi:[0,1]
	v_pk_add_f32 v[50:51], v[42:43], v[58:59]
	v_pk_add_f32 v[42:43], v[42:43], v[58:59] neg_lo:[0,1] neg_hi:[0,1]
	v_pk_add_f32 v[58:59], v[40:41], v[50:51]
	v_pk_add_f32 v[40:41], v[40:41], v[50:51] neg_lo:[0,1] neg_hi:[0,1]
	v_pk_add_f32 v[50:51], v[34:35], v[42:43] op_sel:[0,1] op_sel_hi:[1,0] neg_hi:[0,1]
	v_pk_add_f32 v[34:35], v[34:35], v[42:43] op_sel:[0,1] op_sel_hi:[1,0] neg_lo:[0,1]
	v_pk_add_f32 v[42:43], v[36:37], v[52:53]
	v_pk_add_f32 v[36:37], v[36:37], v[52:53] neg_lo:[0,1] neg_hi:[0,1]
	v_pk_add_f32 v[52:53], v[44:45], v[60:61]
	v_pk_add_f32 v[44:45], v[44:45], v[60:61] neg_lo:[0,1] neg_hi:[0,1]
	v_pk_add_f32 v[60:61], v[42:43], v[52:53]
	v_pk_add_f32 v[42:43], v[42:43], v[52:53] neg_lo:[0,1] neg_hi:[0,1]
	v_pk_add_f32 v[52:53], v[36:37], v[44:45] op_sel:[0,1] op_sel_hi:[1,0] neg_hi:[0,1]
	v_pk_add_f32 v[36:37], v[36:37], v[44:45] op_sel:[0,1] op_sel_hi:[1,0] neg_lo:[0,1]
	v_pk_add_f32 v[44:45], v[38:39], v[54:55]
	v_pk_add_f32 v[38:39], v[38:39], v[54:55] neg_lo:[0,1] neg_hi:[0,1]
	v_pk_add_f32 v[54:55], v[46:47], v[62:63]
	v_pk_add_f32 v[46:47], v[46:47], v[62:63] neg_lo:[0,1] neg_hi:[0,1]
	v_pk_add_f32 v[62:63], v[44:45], v[54:55]
	v_pk_add_f32 v[44:45], v[44:45], v[54:55] neg_lo:[0,1] neg_hi:[0,1]
	v_pk_add_f32 v[54:55], v[38:39], v[46:47] op_sel:[0,1] op_sel_hi:[1,0] neg_hi:[0,1]
	v_pk_add_f32 v[38:39], v[38:39], v[46:47] op_sel:[0,1] op_sel_hi:[1,0] neg_lo:[0,1]
	v_pk_mul_f32 v[46:47], v[50:51], s[6:7] op_sel:[0,0] op_sel_hi:[0,1]
	v_pk_fma_f32 v[46:47], v[50:51], s[6:7], v[46:47] op_sel:[1,1,0] op_sel_hi:[1,0,1] neg_lo:[0,1,0]
	v_pk_mul_f32 v[50:51], v[34:35], s[10:11] op_sel:[0,0] op_sel_hi:[0,1]
	v_pk_fma_f32 v[50:51], v[34:35], s[10:11], v[50:51] op_sel:[1,1,0] op_sel_hi:[1,0,1] neg_lo:[0,1,0]
	v_pk_add_f32 v[34:35], v[52:53], v[52:53] op_sel:[0,1] op_sel_hi:[1,0] neg_hi:[0,1]
	v_pk_add_f32 v[40:41], v[40:41], v[40:41] op_sel:[0,1] op_sel_hi:[1,0] neg_hi:[0,1]
	s_nop 0
	v_pk_mul_f32 v[52:53], v[54:55], s[10:11] op_sel:[0,0] op_sel_hi:[0,1]
	v_pk_fma_f32 v[52:53], v[54:55], s[10:11], v[52:53] op_sel:[1,1,0] op_sel_hi:[1,0,1] neg_lo:[0,1,0]
	v_pk_mul_f32 v[54:55], v[38:39], s[14:15] op_sel:[0,0] op_sel_hi:[0,1]
	v_pk_fma_f32 v[54:55], v[38:39], s[14:15], v[54:55] op_sel:[1,1,0] op_sel_hi:[1,0,1] neg_lo:[0,1,0]
	v_pk_add_f32 v[38:39], v[56:57], v[60:61]
	v_pk_mul_f32 v[34:35], v[34:35], s[8:9]
	v_pk_add_f32 v[56:57], v[56:57], v[60:61] neg_lo:[0,1] neg_hi:[0,1]
	v_pk_add_f32 v[60:61], v[58:59], v[62:63]
	v_pk_add_f32 v[58:59], v[58:59], v[62:63] neg_lo:[0,1] neg_hi:[0,1]
	v_pk_mul_f32 v[40:41], v[40:41], s[8:9]
	v_pk_add_f32 v[36:37], v[36:37], v[36:37] op_sel:[0,1] op_sel_hi:[1,0] neg_lo:[0,1]
	v_pk_add_f32 v[44:45], v[44:45], v[44:45] op_sel:[0,1] op_sel_hi:[1,0] neg_lo:[0,1]
	v_pk_add_f32 v[62:63], v[38:39], v[60:61]
	v_pk_add_f32 v[38:39], v[38:39], v[60:61] neg_lo:[0,1] neg_hi:[0,1]
	v_pk_add_f32 v[60:61], v[56:57], v[58:59] op_sel:[0,1] op_sel_hi:[1,0] neg_hi:[0,1]
	v_pk_add_f32 v[56:57], v[56:57], v[58:59] op_sel:[0,1] op_sel_hi:[1,0] neg_lo:[0,1]
	v_pk_add_f32 v[58:59], v[64:65], v[34:35]
	v_pk_add_f32 v[34:35], v[64:65], v[34:35] neg_lo:[0,1] neg_hi:[0,1]
	v_pk_add_f32 v[64:65], v[46:47], v[52:53]
	v_pk_add_f32 v[46:47], v[46:47], v[52:53] neg_lo:[0,1] neg_hi:[0,1]
	v_pk_mul_f32 v[36:37], v[36:37], s[12:13]
	v_pk_mul_f32 v[44:45], v[44:45], s[12:13]
	v_pk_add_f32 v[52:53], v[58:59], v[64:65]
	v_pk_add_f32 v[58:59], v[58:59], v[64:65] neg_lo:[0,1] neg_hi:[0,1]
	v_pk_add_f32 v[64:65], v[34:35], v[46:47] op_sel:[0,1] op_sel_hi:[1,0] neg_hi:[0,1]
	v_pk_add_f32 v[34:35], v[34:35], v[46:47] op_sel:[0,1] op_sel_hi:[1,0] neg_lo:[0,1]
	v_pk_add_f32 v[46:47], v[48:49], v[42:43] op_sel:[0,1] op_sel_hi:[1,0] neg_hi:[0,1]
	v_pk_add_f32 v[42:43], v[48:49], v[42:43] op_sel:[0,1] op_sel_hi:[1,0] neg_lo:[0,1]
	v_pk_add_f32 v[48:49], v[40:41], v[44:45]
	v_pk_add_f32 v[40:41], v[40:41], v[44:45] neg_lo:[0,1] neg_hi:[0,1]
	v_pk_add_f32 v[44:45], v[48:49], v[46:47]
	v_pk_add_f32 v[46:47], v[46:47], v[48:49] neg_lo:[0,1] neg_hi:[0,1]
	v_pk_add_f32 v[48:49], v[42:43], v[40:41] op_sel:[0,1] op_sel_hi:[1,0] neg_hi:[0,1]
	v_pk_add_f32 v[40:41], v[42:43], v[40:41] op_sel:[0,1] op_sel_hi:[1,0] neg_lo:[0,1]
	v_pk_add_f32 v[42:43], v[32:33], v[36:37]
	v_pk_add_f32 v[32:33], v[32:33], v[36:37] neg_lo:[0,1] neg_hi:[0,1]
	v_pk_add_f32 v[36:37], v[50:51], v[54:55]
	v_pk_add_f32 v[50:51], v[50:51], v[54:55] neg_lo:[0,1] neg_hi:[0,1]
	v_pk_add_f32 v[54:55], v[42:43], v[36:37]
	v_pk_add_f32 v[36:37], v[42:43], v[36:37] neg_lo:[0,1] neg_hi:[0,1]
	v_pk_add_f32 v[42:43], v[32:33], v[50:51] op_sel:[0,1] op_sel_hi:[1,0] neg_hi:[0,1]
	v_pk_add_f32 v[32:33], v[32:33], v[50:51] op_sel:[0,1] op_sel_hi:[1,0] neg_lo:[0,1]
	s_waitcnt vmcnt(0)
	v_pk_mul_f32 v[26:27], v[30:31], v[28:29] op_sel:[0,0] op_sel_hi:[0,1]
	v_pk_fma_f32 v[26:27], v[30:31], v[28:29], v[26:27] op_sel:[1,1,0] op_sel_hi:[1,0,1] neg_lo:[0,1,0]
	v_pk_mul_f32 v[20:21], v[30:31], v[24:25] op_sel:[0,0] op_sel_hi:[0,1]
	v_pk_fma_f32 v[20:21], v[30:31], v[24:25], v[20:21] op_sel:[1,1,0] op_sel_hi:[1,0,1] neg_lo:[0,1,0]
	v_pk_mul_f32 v[16:17], v[28:29], v[24:25] op_sel:[0,0] op_sel_hi:[0,1]
	v_pk_fma_f32 v[16:17], v[28:29], v[24:25], v[16:17] op_sel:[1,1,0] op_sel_hi:[1,0,1] neg_lo:[0,1,0]
	v_pk_mul_f32 v[18:19], v[30:31], v[22:23] op_sel:[0,0] op_sel_hi:[0,1]
	v_pk_fma_f32 v[18:19], v[30:31], v[22:23], v[18:19] op_sel:[1,1,0] op_sel_hi:[1,0,1] neg_lo:[0,1,0]
	v_pk_mul_f32 v[12:13], v[28:29], v[22:23] op_sel:[0,0] op_sel_hi:[0,1]
	v_pk_fma_f32 v[12:13], v[28:29], v[22:23], v[12:13] op_sel:[1,1,0] op_sel_hi:[1,0,1] neg_lo:[0,1,0]
	v_pk_mul_f32 v[6:7], v[24:25], v[22:23] op_sel:[0,0] op_sel_hi:[0,1]
	v_pk_fma_f32 v[6:7], v[24:25], v[22:23], v[6:7] op_sel:[1,1,0] op_sel_hi:[1,0,1] neg_lo:[0,1,0]
	v_pk_mul_f32 v[10:11], v[26:27], v[24:25] op_sel:[0,0] op_sel_hi:[0,1]
	v_pk_fma_f32 v[10:11], v[26:27], v[24:25], v[10:11] op_sel:[1,1,0] op_sel_hi:[1,0,1] neg_lo:[0,1,0]
	v_pk_mul_f32 v[14:15], v[26:27], v[22:23] op_sel:[0,0] op_sel_hi:[0,1]
	v_pk_fma_f32 v[14:15], v[26:27], v[22:23], v[14:15] op_sel:[1,1,0] op_sel_hi:[1,0,1] neg_lo:[0,1,0]
	v_pk_mul_f32 v[8:9], v[20:21], v[22:23] op_sel:[0,0] op_sel_hi:[0,1]
	v_pk_fma_f32 v[8:9], v[20:21], v[22:23], v[8:9] op_sel:[1,1,0] op_sel_hi:[1,0,1] neg_lo:[0,1,0]
	v_pk_mul_f32 v[4:5], v[16:17], v[22:23] op_sel:[0,0] op_sel_hi:[0,1]
	v_pk_fma_f32 v[4:5], v[16:17], v[22:23], v[4:5] op_sel:[1,1,0] op_sel_hi:[1,0,1] neg_lo:[0,1,0]
	v_pk_mul_f32 v[2:3], v[10:11], v[22:23] op_sel:[0,0] op_sel_hi:[0,1]
	v_pk_fma_f32 v[2:3], v[10:11], v[22:23], v[2:3] op_sel:[1,1,0] op_sel_hi:[1,0,1] neg_lo:[0,1,0]
	v_pk_mul_f32 v[50:51], v[52:53], v[30:31] op_sel:[0,0] op_sel_hi:[0,1]
	v_pk_fma_f32 v[50:51], v[52:53], v[30:31], v[50:51] op_sel:[1,1,0] op_sel_hi:[1,0,1] neg_lo:[0,1,0]
	ds_write_b64 v1, v[50:51] offset:2184
	v_pk_mul_f32 v[50:51], v[44:45], v[28:29] op_sel:[0,0] op_sel_hi:[0,1]
	v_pk_fma_f32 v[50:51], v[44:45], v[28:29], v[50:51] op_sel:[1,1,0] op_sel_hi:[1,0,1] neg_lo:[0,1,0]
	v_pk_mul_f32 v[44:45], v[54:55], v[26:27] op_sel:[0,0] op_sel_hi:[0,1]
	v_pk_fma_f32 v[44:45], v[54:55], v[26:27], v[44:45] op_sel:[1,1,0] op_sel_hi:[1,0,1] neg_lo:[0,1,0]
	ds_write_b64 v1, v[44:45] offset:6552
	v_pk_mul_f32 v[44:45], v[60:61], v[24:25] op_sel:[0,0] op_sel_hi:[0,1]
	v_pk_fma_f32 v[44:45], v[60:61], v[24:25], v[44:45] op_sel:[1,1,0] op_sel_hi:[1,0,1] neg_lo:[0,1,0]
	ds_write_b64 v1, v[44:45] offset:8736
	v_pk_mul_f32 v[44:45], v[64:65], v[20:21] op_sel:[0,0] op_sel_hi:[0,1]
	v_pk_fma_f32 v[44:45], v[64:65], v[20:21], v[44:45] op_sel:[1,1,0] op_sel_hi:[1,0,1] neg_lo:[0,1,0]
	ds_write_b64 v1, v[44:45] offset:10920
	v_pk_mul_f32 v[44:45], v[48:49], v[16:17] op_sel:[0,0] op_sel_hi:[0,1]
	v_pk_fma_f32 v[44:45], v[48:49], v[16:17], v[44:45] op_sel:[1,1,0] op_sel_hi:[1,0,1] neg_lo:[0,1,0]
	ds_write_b64 v1, v[44:45] offset:13104
	v_pk_mul_f32 v[44:45], v[42:43], v[10:11] op_sel:[0,0] op_sel_hi:[0,1]
	v_pk_fma_f32 v[44:45], v[42:43], v[10:11], v[44:45] op_sel:[1,1,0] op_sel_hi:[1,0,1] neg_lo:[0,1,0]
	v_pk_mul_f32 v[42:43], v[38:39], v[22:23] op_sel:[0,0] op_sel_hi:[0,1]
	v_pk_fma_f32 v[42:43], v[38:39], v[22:23], v[42:43] op_sel:[1,1,0] op_sel_hi:[1,0,1] neg_lo:[0,1,0]
	v_pk_mul_f32 v[38:39], v[58:59], v[18:19] op_sel:[0,0] op_sel_hi:[0,1]
	v_pk_fma_f32 v[38:39], v[58:59], v[18:19], v[38:39] op_sel:[1,1,0] op_sel_hi:[1,0,1] neg_lo:[0,1,0]
	ds_write_b64 v1, v[38:39] offset:19656
	v_pk_mul_f32 v[38:39], v[46:47], v[12:13] op_sel:[0,0] op_sel_hi:[0,1]
	v_pk_fma_f32 v[38:39], v[46:47], v[12:13], v[38:39] op_sel:[1,1,0] op_sel_hi:[1,0,1] neg_lo:[0,1,0]
	ds_write_b64 v1, v[38:39] offset:21840
	v_pk_mul_f32 v[38:39], v[36:37], v[14:15] op_sel:[0,0] op_sel_hi:[0,1]
	v_pk_fma_f32 v[38:39], v[36:37], v[14:15], v[38:39] op_sel:[1,1,0] op_sel_hi:[1,0,1] neg_lo:[0,1,0]
	v_pk_mul_f32 v[36:37], v[56:57], v[6:7] op_sel:[0,0] op_sel_hi:[0,1]
	v_pk_fma_f32 v[36:37], v[56:57], v[6:7], v[36:37] op_sel:[1,1,0] op_sel_hi:[1,0,1] neg_lo:[0,1,0]
	ds_write_b64 v1, v[36:37] offset:26208
	v_pk_mul_f32 v[36:37], v[34:35], v[8:9] op_sel:[0,0] op_sel_hi:[0,1]
	v_pk_fma_f32 v[36:37], v[34:35], v[8:9], v[36:37] op_sel:[1,1,0] op_sel_hi:[1,0,1] neg_lo:[0,1,0]
	v_pk_mul_f32 v[34:35], v[40:41], v[4:5] op_sel:[0,0] op_sel_hi:[0,1]
	v_pk_fma_f32 v[34:35], v[40:41], v[4:5], v[34:35] op_sel:[1,1,0] op_sel_hi:[1,0,1] neg_lo:[0,1,0]
	ds_write_b64 v1, v[34:35] offset:30576
	v_pk_mul_f32 v[34:35], v[32:33], v[2:3] op_sel:[0,0] op_sel_hi:[0,1]
	v_pk_fma_f32 v[34:35], v[32:33], v[2:3], v[34:35] op_sel:[1,1,0] op_sel_hi:[1,0,1] neg_lo:[0,1,0]
	ds_write_b64 v1, v[62:63]
	ds_write_b64 v1, v[50:51] offset:4368
	ds_write_b64 v1, v[44:45] offset:15288
	ds_write_b64 v1, v[42:43] offset:17472
	ds_write_b64 v1, v[38:39] offset:24024
	ds_write_b64 v1, v[36:37] offset:28392
	ds_write_b64 v1, v[34:35] offset:32760
	ds_write_b64 v1, v[86:87] offset:34816
	s_waitcnt lgkmcnt(0)
	s_barrier
	ds_read2_b64 v[32:35], v96 offset1:16
	ds_read2_b64 v[36:39], v96 offset0:32 offset1:48
	ds_read2_b64 v[40:43], v96 offset0:64 offset1:80
	ds_read2_b64 v[44:47], v96 offset0:128 offset1:144
	ds_read2_b64 v[48:51], v96 offset0:96 offset1:112
	ds_read2_b64 v[52:55], v96 offset0:192 offset1:208
	ds_read2_b64 v[56:59], v96 offset0:160 offset1:176
	ds_read2_b64 v[60:63], v96 offset0:224 offset1:240
	v_lshlrev_b32_e32 v115, 2, v0
	v_lshlrev_b32_e32 v119, 2, v0
	v_lshlrev_b32_e32 v123, 2, v0
	v_lshlrev_b32_e32 v127, 2, v0
	v_or_b32_e32 v119, 0x1000, v119
	v_or_b32_e32 v123, 0x2000, v123
	v_or_b32_e32 v127, 0x3000, v127
	global_load_ushort v112, v115, s[20:21]
	global_load_ushort v113, v115, s[20:21] offset:1024
	global_load_ushort v114, v115, s[20:21] offset:2048
	global_load_ushort v115, v115, s[20:21] offset:3072
	global_load_ushort v116, v119, s[20:21]
	global_load_ushort v117, v119, s[20:21] offset:1024
	global_load_ushort v118, v119, s[20:21] offset:2048
	global_load_ushort v119, v119, s[20:21] offset:3072
	global_load_ushort v120, v123, s[20:21]
	global_load_ushort v121, v123, s[20:21] offset:1024
	global_load_ushort v122, v123, s[20:21] offset:2048
	global_load_ushort v123, v123, s[20:21] offset:3072
	global_load_ushort v124, v127, s[20:21]
	global_load_ushort v125, v127, s[20:21] offset:1024
	global_load_ushort v126, v127, s[20:21] offset:2048
	global_load_ushort v127, v127, s[20:21] offset:3072
	s_waitcnt lgkmcnt(4)
	v_pk_add_f32 v[64:65], v[32:33], v[44:45]
	v_pk_add_f32 v[32:33], v[32:33], v[44:45] neg_lo:[0,1] neg_hi:[0,1]
	s_waitcnt lgkmcnt(2)
	v_pk_add_f32 v[44:45], v[40:41], v[52:53]
	v_pk_add_f32 v[40:41], v[40:41], v[52:53] neg_lo:[0,1] neg_hi:[0,1]
	v_pk_add_f32 v[52:53], v[64:65], v[44:45]
	v_pk_add_f32 v[44:45], v[64:65], v[44:45] neg_lo:[0,1] neg_hi:[0,1]
	v_pk_add_f32 v[64:65], v[32:33], v[40:41] op_sel:[0,1] op_sel_hi:[1,0] neg_hi:[0,1]
	v_pk_add_f32 v[32:33], v[32:33], v[40:41] op_sel:[0,1] op_sel_hi:[1,0] neg_lo:[0,1]
	v_pk_add_f32 v[40:41], v[34:35], v[46:47]
	v_pk_add_f32 v[34:35], v[34:35], v[46:47] neg_lo:[0,1] neg_hi:[0,1]
	v_pk_add_f32 v[46:47], v[42:43], v[54:55]
	v_pk_add_f32 v[42:43], v[42:43], v[54:55] neg_lo:[0,1] neg_hi:[0,1]
	v_pk_add_f32 v[54:55], v[40:41], v[46:47]
	v_pk_add_f32 v[40:41], v[40:41], v[46:47] neg_lo:[0,1] neg_hi:[0,1]
	v_pk_add_f32 v[46:47], v[34:35], v[42:43] op_sel:[0,1] op_sel_hi:[1,0] neg_hi:[0,1]
	v_pk_add_f32 v[34:35], v[34:35], v[42:43] op_sel:[0,1] op_sel_hi:[1,0] neg_lo:[0,1]
	s_waitcnt lgkmcnt(1)
	v_pk_add_f32 v[42:43], v[36:37], v[56:57]
	v_pk_add_f32 v[36:37], v[36:37], v[56:57] neg_lo:[0,1] neg_hi:[0,1]
	s_waitcnt lgkmcnt(0)
	v_pk_add_f32 v[56:57], v[48:49], v[60:61]
	v_pk_add_f32 v[48:49], v[48:49], v[60:61] neg_lo:[0,1] neg_hi:[0,1]
	v_pk_add_f32 v[60:61], v[42:43], v[56:57]
	v_pk_add_f32 v[42:43], v[42:43], v[56:57] neg_lo:[0,1] neg_hi:[0,1]
	v_pk_add_f32 v[56:57], v[36:37], v[48:49] op_sel:[0,1] op_sel_hi:[1,0] neg_hi:[0,1]
	v_pk_add_f32 v[36:37], v[36:37], v[48:49] op_sel:[0,1] op_sel_hi:[1,0] neg_lo:[0,1]
	v_pk_add_f32 v[48:49], v[38:39], v[58:59]
	v_pk_add_f32 v[38:39], v[38:39], v[58:59] neg_lo:[0,1] neg_hi:[0,1]
	v_pk_add_f32 v[58:59], v[50:51], v[62:63]
	v_pk_add_f32 v[50:51], v[50:51], v[62:63] neg_lo:[0,1] neg_hi:[0,1]
	v_pk_add_f32 v[62:63], v[48:49], v[58:59]
	v_pk_add_f32 v[48:49], v[48:49], v[58:59] neg_lo:[0,1] neg_hi:[0,1]
	v_pk_add_f32 v[58:59], v[38:39], v[50:51] op_sel:[0,1] op_sel_hi:[1,0] neg_hi:[0,1]
	v_pk_add_f32 v[38:39], v[38:39], v[50:51] op_sel:[0,1] op_sel_hi:[1,0] neg_lo:[0,1]
	v_pk_mul_f32 v[50:51], v[46:47], s[6:7] op_sel:[0,0] op_sel_hi:[0,1]
	v_pk_fma_f32 v[50:51], v[46:47], s[6:7], v[50:51] op_sel:[1,1,0] op_sel_hi:[1,0,1] neg_lo:[0,1,0]
	v_pk_mul_f32 v[46:47], v[34:35], s[10:11] op_sel:[0,0] op_sel_hi:[0,1]
	v_pk_fma_f32 v[46:47], v[34:35], s[10:11], v[46:47] op_sel:[1,1,0] op_sel_hi:[1,0,1] neg_lo:[0,1,0]
	v_pk_add_f32 v[34:35], v[56:57], v[56:57] op_sel:[0,1] op_sel_hi:[1,0] neg_hi:[0,1]
	v_pk_add_f32 v[40:41], v[40:41], v[40:41] op_sel:[0,1] op_sel_hi:[1,0] neg_hi:[0,1]
	s_nop 0
	v_pk_mul_f32 v[56:57], v[58:59], s[10:11] op_sel:[0,0] op_sel_hi:[0,1]
	v_pk_fma_f32 v[56:57], v[58:59], s[10:11], v[56:57] op_sel:[1,1,0] op_sel_hi:[1,0,1] neg_lo:[0,1,0]
	v_pk_mul_f32 v[58:59], v[38:39], s[14:15] op_sel:[0,0] op_sel_hi:[0,1]
	v_pk_fma_f32 v[58:59], v[38:39], s[14:15], v[58:59] op_sel:[1,1,0] op_sel_hi:[1,0,1] neg_lo:[0,1,0]
	v_pk_add_f32 v[38:39], v[52:53], v[60:61]
	v_pk_mul_f32 v[34:35], v[34:35], s[8:9]
	v_pk_add_f32 v[52:53], v[52:53], v[60:61] neg_lo:[0,1] neg_hi:[0,1]
	v_pk_add_f32 v[60:61], v[54:55], v[62:63]
	v_pk_add_f32 v[54:55], v[54:55], v[62:63] neg_lo:[0,1] neg_hi:[0,1]
	v_pk_add_f32 v[36:37], v[36:37], v[36:37] op_sel:[0,1] op_sel_hi:[1,0] neg_lo:[0,1]
	v_pk_add_f32 v[48:49], v[48:49], v[48:49] op_sel:[0,1] op_sel_hi:[1,0] neg_lo:[0,1]
	v_pk_add_f32 v[62:63], v[38:39], v[60:61]
	v_pk_add_f32 v[60:61], v[38:39], v[60:61] neg_lo:[0,1] neg_hi:[0,1]
	v_pk_add_f32 v[66:67], v[52:53], v[54:55] op_sel:[0,1] op_sel_hi:[1,0] neg_hi:[0,1]
	v_pk_add_f32 v[52:53], v[52:53], v[54:55] op_sel:[0,1] op_sel_hi:[1,0] neg_lo:[0,1]
	v_pk_add_f32 v[38:39], v[64:65], v[34:35]
	v_pk_add_f32 v[34:35], v[64:65], v[34:35] neg_lo:[0,1] neg_hi:[0,1]
	v_pk_add_f32 v[54:55], v[50:51], v[56:57]
	v_pk_add_f32 v[50:51], v[50:51], v[56:57] neg_lo:[0,1] neg_hi:[0,1]
	v_pk_mul_f32 v[40:41], v[40:41], s[8:9]
	v_pk_mul_f32 v[36:37], v[36:37], s[12:13]
	v_pk_mul_f32 v[48:49], v[48:49], s[12:13]
	v_pk_add_f32 v[56:57], v[38:39], v[54:55]
	v_pk_add_f32 v[54:55], v[38:39], v[54:55] neg_lo:[0,1] neg_hi:[0,1]
	v_pk_add_f32 v[64:65], v[34:35], v[50:51] op_sel:[0,1] op_sel_hi:[1,0] neg_hi:[0,1]
	v_pk_add_f32 v[50:51], v[34:35], v[50:51] op_sel:[0,1] op_sel_hi:[1,0] neg_lo:[0,1]
	v_pk_add_f32 v[34:35], v[44:45], v[42:43] op_sel:[0,1] op_sel_hi:[1,0] neg_hi:[0,1]
	v_pk_add_f32 v[38:39], v[44:45], v[42:43] op_sel:[0,1] op_sel_hi:[1,0] neg_lo:[0,1]
	v_pk_add_f32 v[42:43], v[40:41], v[48:49]
	v_pk_add_f32 v[40:41], v[40:41], v[48:49] neg_lo:[0,1] neg_hi:[0,1]
	v_pk_add_f32 v[44:45], v[42:43], v[34:35]
	v_pk_add_f32 v[42:43], v[34:35], v[42:43] neg_lo:[0,1] neg_hi:[0,1]
	v_pk_add_f32 v[34:35], v[32:33], v[36:37]
	v_pk_add_f32 v[36:37], v[32:33], v[36:37] neg_lo:[0,1] neg_hi:[0,1]
	v_pk_add_f32 v[32:33], v[46:47], v[58:59]
	v_pk_add_f32 v[48:49], v[38:39], v[40:41] op_sel:[0,1] op_sel_hi:[1,0] neg_hi:[0,1]
	v_pk_add_f32 v[40:41], v[38:39], v[40:41] op_sel:[0,1] op_sel_hi:[1,0] neg_lo:[0,1]
	v_pk_add_f32 v[38:39], v[46:47], v[58:59] neg_lo:[0,1] neg_hi:[0,1]
	v_pk_add_f32 v[46:47], v[34:35], v[32:33]
	v_pk_add_f32 v[58:59], v[34:35], v[32:33] neg_lo:[0,1] neg_hi:[0,1]
	v_pk_add_f32 v[68:69], v[36:37], v[38:39] op_sel:[0,1] op_sel_hi:[1,0] neg_hi:[0,1]
	v_pk_add_f32 v[86:87], v[36:37], v[38:39] op_sel:[0,1] op_sel_hi:[1,0] neg_lo:[0,1]
	s_nop 0
	v_ashrrev_i32_e32 v32, 4, v88
	v_lshlrev_b32_e32 v90, 3, v32
	v_add_u32_e32 v91, 0x8800, v90
	v_and_b32_e32 v36, 15, v88
	ds_read2_b64 v[32:35], v91 offset0:16 offset1:32
	v_mad_u32_u24 v92, v36, s5, v90
	ds_read2_b64 v[36:39], v91 offset0:48 offset1:64
	s_waitcnt lgkmcnt(1)
	v_pk_mul_f32 v[88:89], v[56:57], v[32:33] op_sel:[0,0] op_sel_hi:[0,1]
	v_pk_fma_f32 v[88:89], v[56:57], v[32:33], v[88:89] op_sel:[1,1,0] op_sel_hi:[1,0,1] neg_lo:[0,1,0]
	v_pk_mul_f32 v[56:57], v[44:45], v[34:35] op_sel:[0,0] op_sel_hi:[0,1]
	v_pk_fma_f32 v[56:57], v[44:45], v[34:35], v[56:57] op_sel:[1,1,0] op_sel_hi:[1,0,1] neg_lo:[0,1,0]
	s_waitcnt lgkmcnt(0)
	v_pk_mul_f32 v[44:45], v[46:47], v[36:37] op_sel:[0,0] op_sel_hi:[0,1]
	v_pk_fma_f32 v[44:45], v[46:47], v[36:37], v[44:45] op_sel:[1,1,0] op_sel_hi:[1,0,1] neg_lo:[0,1,0]
	ds_write2_b64 v92, v[56:57], v[44:45] offset0:32 offset1:48
	v_pk_mul_f32 v[44:45], v[66:67], v[38:39] op_sel:[0,0] op_sel_hi:[0,1]
	v_pk_fma_f32 v[44:45], v[66:67], v[38:39], v[44:45] op_sel:[1,1,0] op_sel_hi:[1,0,1] neg_lo:[0,1,0]
	ds_read2_b64 v[32:35], v91 offset0:80 offset1:96
	s_waitcnt lgkmcnt(0)
	v_pk_mul_f32 v[46:47], v[64:65], v[32:33] op_sel:[0,0] op_sel_hi:[0,1]
	v_pk_fma_f32 v[46:47], v[64:65], v[32:33], v[46:47] op_sel:[1,1,0] op_sel_hi:[1,0,1] neg_lo:[0,1,0]
	ds_write2_b64 v92, v[44:45], v[46:47] offset0:64 offset1:80
	v_pk_mul_f32 v[44:45], v[48:49], v[34:35] op_sel:[0,0] op_sel_hi:[0,1]
	v_pk_fma_f32 v[44:45], v[48:49], v[34:35], v[44:45] op_sel:[1,1,0] op_sel_hi:[1,0,1] neg_lo:[0,1,0]
	ds_read2_b64 v[36:39], v91 offset0:112 offset1:128
	ds_read2_b64 v[32:35], v91 offset0:144 offset1:160
	s_waitcnt lgkmcnt(1)
	v_pk_mul_f32 v[46:47], v[68:69], v[36:37] op_sel:[0,0] op_sel_hi:[0,1]
	v_pk_fma_f32 v[46:47], v[68:69], v[36:37], v[46:47] op_sel:[1,1,0] op_sel_hi:[1,0,1] neg_lo:[0,1,0]
	ds_write2_b64 v92, v[44:45], v[46:47] offset0:96 offset1:112
	v_pk_mul_f32 v[44:45], v[60:61], v[38:39] op_sel:[0,0] op_sel_hi:[0,1]
	v_pk_fma_f32 v[44:45], v[60:61], v[38:39], v[44:45] op_sel:[1,1,0] op_sel_hi:[1,0,1] neg_lo:[0,1,0]
	ds_read2_b64 v[36:39], v91 offset0:176 offset1:192
	s_waitcnt lgkmcnt(2)
	v_pk_mul_f32 v[46:47], v[54:55], v[32:33] op_sel:[0,0] op_sel_hi:[0,1]
	v_pk_fma_f32 v[46:47], v[54:55], v[32:33], v[46:47] op_sel:[1,1,0] op_sel_hi:[1,0,1] neg_lo:[0,1,0]
	ds_write2_b64 v92, v[44:45], v[46:47] offset0:128 offset1:144
	v_pk_mul_f32 v[44:45], v[42:43], v[34:35] op_sel:[0,0] op_sel_hi:[0,1]
	v_pk_fma_f32 v[44:45], v[42:43], v[34:35], v[44:45] op_sel:[1,1,0] op_sel_hi:[1,0,1] neg_lo:[0,1,0]
	ds_read2_b64 v[32:35], v91 offset0:208 offset1:224
	s_waitcnt lgkmcnt(2)
	v_pk_mul_f32 v[42:43], v[58:59], v[36:37] op_sel:[0,0] op_sel_hi:[0,1]
	v_pk_fma_f32 v[42:43], v[58:59], v[36:37], v[42:43] op_sel:[1,1,0] op_sel_hi:[1,0,1] neg_lo:[0,1,0]
	ds_write2_b64 v92, v[44:45], v[42:43] offset0:160 offset1:176
	v_pk_mul_f32 v[42:43], v[52:53], v[38:39] op_sel:[0,0] op_sel_hi:[0,1]
	v_pk_fma_f32 v[42:43], v[52:53], v[38:39], v[42:43] op_sel:[1,1,0] op_sel_hi:[1,0,1] neg_lo:[0,1,0]
	s_waitcnt lgkmcnt(1)
	v_pk_mul_f32 v[38:39], v[50:51], v[32:33] op_sel:[0,0] op_sel_hi:[0,1]
	v_pk_fma_f32 v[38:39], v[50:51], v[32:33], v[38:39] op_sel:[1,1,0] op_sel_hi:[1,0,1] neg_lo:[0,1,0]
	v_pk_mul_f32 v[32:33], v[40:41], v[34:35] op_sel:[0,0] op_sel_hi:[0,1]
	v_pk_fma_f32 v[32:33], v[40:41], v[34:35], v[32:33] op_sel:[1,1,0] op_sel_hi:[1,0,1] neg_lo:[0,1,0]
	ds_read_b64 v[36:37], v90 offset:36736
	s_waitcnt lgkmcnt(0)
	v_pk_mul_f32 v[34:35], v[86:87], v[36:37] op_sel:[0,0] op_sel_hi:[0,1]
	v_pk_fma_f32 v[34:35], v[86:87], v[36:37], v[34:35] op_sel:[1,1,0] op_sel_hi:[1,0,1] neg_lo:[0,1,0]
	ds_write2_b64 v92, v[32:33], v[34:35] offset0:224 offset1:240
	v_mov_b32_e32 v32, v0
	ds_write2_b64 v92, v[62:63], v[88:89] offset1:16
	ds_write2_b64 v92, v[42:43], v[38:39] offset0:192 offset1:208
	s_waitcnt lgkmcnt(0)
	s_barrier
	s_nop 0
	v_and_b32_e32 v33, 15, v32
	v_and_b32_e32 v32, 0x1ffffff0, v32
	v_lshlrev_b32_e32 v32, 3, v32
	v_mad_u32_u24 v60, v33, s5, v32
	ds_read2_b64 v[32:35], v60 offset1:1
	ds_read2_b64 v[36:39], v60 offset0:2 offset1:3
	ds_read2_b64 v[40:43], v60 offset0:8 offset1:9
	ds_read2_b64 v[44:47], v60 offset0:4 offset1:5
	ds_read2_b64 v[48:51], v60 offset0:6 offset1:7
	ds_read2_b64 v[52:55], v60 offset0:12 offset1:13
	ds_read2_b64 v[56:59], v60 offset0:10 offset1:11
	ds_read2_b64 v[60:63], v60 offset0:14 offset1:15
	s_waitcnt lgkmcnt(5)
	v_pk_add_f32 v[64:65], v[32:33], v[40:41]
	v_pk_add_f32 v[32:33], v[32:33], v[40:41] neg_lo:[0,1] neg_hi:[0,1]
	s_waitcnt lgkmcnt(2)
	v_pk_add_f32 v[40:41], v[44:45], v[52:53]
	v_pk_add_f32 v[44:45], v[44:45], v[52:53] neg_lo:[0,1] neg_hi:[0,1]
	v_pk_add_f32 v[52:53], v[64:65], v[40:41]
	v_pk_add_f32 v[40:41], v[64:65], v[40:41] neg_lo:[0,1] neg_hi:[0,1]
	v_pk_add_f32 v[64:65], v[32:33], v[44:45] op_sel:[0,1] op_sel_hi:[1,0] neg_hi:[0,1]
	v_pk_add_f32 v[66:67], v[32:33], v[44:45] op_sel:[0,1] op_sel_hi:[1,0] neg_lo:[0,1]
	v_pk_add_f32 v[32:33], v[34:35], v[42:43]
	v_pk_add_f32 v[34:35], v[34:35], v[42:43] neg_lo:[0,1] neg_hi:[0,1]
	v_pk_add_f32 v[42:43], v[46:47], v[54:55]
	v_pk_add_f32 v[44:45], v[46:47], v[54:55] neg_lo:[0,1] neg_hi:[0,1]
	v_pk_add_f32 v[46:47], v[32:33], v[42:43]
	v_pk_add_f32 v[32:33], v[32:33], v[42:43] neg_lo:[0,1] neg_hi:[0,1]
	v_pk_add_f32 v[42:43], v[34:35], v[44:45] op_sel:[0,1] op_sel_hi:[1,0] neg_hi:[0,1]
	v_pk_add_f32 v[34:35], v[34:35], v[44:45] op_sel:[0,1] op_sel_hi:[1,0] neg_lo:[0,1]
	s_waitcnt lgkmcnt(1)
	v_pk_add_f32 v[44:45], v[36:37], v[56:57]
	s_waitcnt lgkmcnt(0)
	v_pk_add_f32 v[54:55], v[48:49], v[60:61]
	v_pk_add_f32 v[32:33], v[32:33], v[32:33] op_sel:[0,1] op_sel_hi:[1,0] neg_hi:[0,1]
	v_pk_add_f32 v[36:37], v[36:37], v[56:57] neg_lo:[0,1] neg_hi:[0,1]
	v_pk_add_f32 v[48:49], v[48:49], v[60:61] neg_lo:[0,1] neg_hi:[0,1]
	v_pk_add_f32 v[56:57], v[44:45], v[54:55]
	v_pk_add_f32 v[54:55], v[44:45], v[54:55] neg_lo:[0,1] neg_hi:[0,1]
	v_pk_add_f32 v[44:45], v[36:37], v[48:49] op_sel:[0,1] op_sel_hi:[1,0] neg_hi:[0,1]
	v_pk_mul_f32 v[68:69], v[32:33], s[8:9]
	v_pk_add_f32 v[36:37], v[36:37], v[48:49] op_sel:[0,1] op_sel_hi:[1,0] neg_lo:[0,1]
	v_pk_add_f32 v[48:49], v[38:39], v[58:59]
	v_pk_add_f32 v[32:33], v[44:45], v[44:45] op_sel:[0,1] op_sel_hi:[1,0] neg_hi:[0,1]
	v_pk_add_f32 v[38:39], v[38:39], v[58:59] neg_lo:[0,1] neg_hi:[0,1]
	v_pk_add_f32 v[58:59], v[50:51], v[62:63]
	v_pk_mul_f32 v[86:87], v[34:35], s[10:11] op_sel:[0,0] op_sel_hi:[0,1]
	v_pk_fma_f32 v[86:87], v[34:35], s[10:11], v[86:87] op_sel:[1,1,0] op_sel_hi:[1,0,1] neg_lo:[0,1,0]
	v_pk_mul_f32 v[34:35], v[32:33], s[8:9]
	v_pk_add_f32 v[32:33], v[36:37], v[36:37] op_sel:[0,1] op_sel_hi:[1,0] neg_lo:[0,1]
	v_pk_add_f32 v[50:51], v[50:51], v[62:63] neg_lo:[0,1] neg_hi:[0,1]
	v_pk_add_f32 v[60:61], v[48:49], v[58:59]
	v_pk_add_f32 v[48:49], v[48:49], v[58:59] neg_lo:[0,1] neg_hi:[0,1]
	v_pk_add_f32 v[58:59], v[38:39], v[50:51] op_sel:[0,1] op_sel_hi:[1,0] neg_hi:[0,1]
	v_pk_add_f32 v[38:39], v[38:39], v[50:51] op_sel:[0,1] op_sel_hi:[1,0] neg_lo:[0,1]
	v_pk_mul_f32 v[88:89], v[32:33], s[12:13]
	v_pk_add_f32 v[36:37], v[46:47], v[60:61]
	v_pk_add_f32 v[32:33], v[48:49], v[48:49] op_sel:[0,1] op_sel_hi:[1,0] neg_lo:[0,1]
	v_pk_mul_f32 v[44:45], v[58:59], s[10:11] op_sel:[0,0] op_sel_hi:[0,1]
	v_pk_fma_f32 v[44:45], v[58:59], s[10:11], v[44:45] op_sel:[1,1,0] op_sel_hi:[1,0,1] neg_lo:[0,1,0]
	v_pk_mul_f32 v[58:59], v[38:39], s[14:15] op_sel:[0,0] op_sel_hi:[0,1]
	v_pk_fma_f32 v[58:59], v[38:39], s[14:15], v[58:59] op_sel:[1,1,0] op_sel_hi:[1,0,1] neg_lo:[0,1,0]
	v_pk_add_f32 v[38:39], v[52:53], v[56:57] neg_lo:[0,1] neg_hi:[0,1]
	v_pk_mul_f32 v[48:49], v[32:33], s[12:13]
	v_pk_add_f32 v[32:33], v[52:53], v[56:57]
	v_pk_add_f32 v[46:47], v[46:47], v[60:61] neg_lo:[0,1] neg_hi:[0,1]
	v_pk_mul_f32 v[62:63], v[42:43], s[6:7] op_sel:[0,0] op_sel_hi:[0,1]
	v_pk_fma_f32 v[62:63], v[42:43], s[6:7], v[62:63] op_sel:[1,1,0] op_sel_hi:[1,0,1] neg_lo:[0,1,0]
	v_pk_add_f32 v[50:51], v[32:33], v[36:37]
	v_pk_add_f32 v[36:37], v[32:33], v[36:37] neg_lo:[0,1] neg_hi:[0,1]
	v_pk_add_f32 v[42:43], v[38:39], v[46:47] op_sel:[0,1] op_sel_hi:[1,0] neg_hi:[0,1]
	v_pk_add_f32 v[32:33], v[38:39], v[46:47] op_sel:[0,1] op_sel_hi:[1,0] neg_lo:[0,1]
	v_pk_add_f32 v[38:39], v[64:65], v[34:35]
	v_pk_add_f32 v[34:35], v[64:65], v[34:35] neg_lo:[0,1] neg_hi:[0,1]
	v_pk_add_f32 v[46:47], v[62:63], v[44:45]
	v_pk_add_f32 v[56:57], v[62:63], v[44:45] neg_lo:[0,1] neg_hi:[0,1]
	v_pk_add_f32 v[52:53], v[38:39], v[46:47]
	v_pk_add_f32 v[38:39], v[38:39], v[46:47] neg_lo:[0,1] neg_hi:[0,1]
	v_pk_add_f32 v[44:45], v[34:35], v[56:57] op_sel:[0,1] op_sel_hi:[1,0] neg_hi:[0,1]
	v_pk_add_f32 v[34:35], v[34:35], v[56:57] op_sel:[0,1] op_sel_hi:[1,0] neg_lo:[0,1]
	v_pk_add_f32 v[46:47], v[40:41], v[54:55] op_sel:[0,1] op_sel_hi:[1,0] neg_hi:[0,1]
	v_pk_add_f32 v[56:57], v[40:41], v[54:55] op_sel:[0,1] op_sel_hi:[1,0] neg_lo:[0,1]
	v_pk_add_f32 v[40:41], v[68:69], v[48:49]
	v_pk_add_f32 v[60:61], v[68:69], v[48:49] neg_lo:[0,1] neg_hi:[0,1]
	v_pk_add_f32 v[54:55], v[40:41], v[46:47]
	v_pk_add_f32 v[40:41], v[46:47], v[40:41] neg_lo:[0,1] neg_hi:[0,1]
	v_pk_add_f32 v[46:47], v[66:67], v[88:89]
	v_pk_add_f32 v[62:63], v[86:87], v[58:59]
	v_pk_add_f32 v[58:59], v[86:87], v[58:59] neg_lo:[0,1] neg_hi:[0,1]
	v_pk_add_f32 v[48:49], v[56:57], v[60:61] op_sel:[0,1] op_sel_hi:[1,0] neg_hi:[0,1]
	v_pk_add_f32 v[64:65], v[56:57], v[60:61] op_sel:[0,1] op_sel_hi:[1,0] neg_lo:[0,1]
	v_pk_add_f32 v[60:61], v[66:67], v[88:89] neg_lo:[0,1] neg_hi:[0,1]
	v_pk_add_f32 v[56:57], v[46:47], v[62:63]
	v_pk_add_f32 v[68:69], v[46:47], v[62:63] neg_lo:[0,1] neg_hi:[0,1]
	v_pk_add_f32 v[46:47], v[60:61], v[58:59] op_sel:[0,1] op_sel_hi:[1,0] neg_hi:[0,1]
	v_pk_add_f32 v[66:67], v[60:61], v[58:59] op_sel:[0,1] op_sel_hi:[1,0] neg_lo:[0,1]
	v_mov_b32_e32 v58, v0
	s_nop 0
	v_and_b32_e32 v59, -16, v58
	v_and_b32_e32 v60, 15, v58
	v_lshlrev_b32_e32 v61, 3, v59
	v_mad_u32_u24 v61, v60, s5, v61
	v_cmp_ne_u32_e32 vcc, 0, v60
	ds_write2_b64 v61, v[50:51], v[52:53] offset1:1
	ds_write2_b64 v61, v[54:55], v[56:57] offset0:2 offset1:3
	ds_write2_b64 v61, v[42:43], v[44:45] offset0:4 offset1:5
	ds_write2_b64 v61, v[48:49], v[46:47] offset0:6 offset1:7
	ds_write2_b64 v61, v[36:37], v[38:39] offset0:8 offset1:9
	ds_write2_b64 v61, v[40:41], v[68:69] offset0:10 offset1:11
	ds_write2_b64 v61, v[32:33], v[34:35] offset0:12 offset1:13
	ds_write2_b64 v61, v[64:65], v[66:67] offset0:14 offset1:15
	s_waitcnt lgkmcnt(0)
	s_barrier
	s_and_saveexec_b64 s[6:7], vcc
	s_xor_b64 s[6:7], exec, s[6:7]
	v_sub_u32_e32 v60, 16, v60
	v_mul_u32_u24_e32 v60, 0x111, v60
	v_sub_u32_e32 v59, v60, v59
	v_add_u32_e32 v61, 0xf0, v59
	s_andn2_saveexec_b64 s[6:7], s[6:7]
	v_sub_u32_e32 v59, 0x100, v58
	v_cmp_lt_u32_e32 vcc, 15, v58
	s_nop 1
	v_cndmask_b32_e32 v61, 1, v59, vcc
	s_or_b64 exec, exec, s[6:7]
	v_mov_b32_e32 v59, 0
	v_lshlrev_b32_e32 v92, 3, v61
	ds_read_b64 v[90:91], v59
	ds_read2_b64 v[60:63], v92 offset0:14 offset1:15
	ds_read2_b64 v[86:89], v92 offset0:12 offset1:13
	v_cmp_eq_u32_e32 vcc, 0, v58
	v_cvt_f32_fp8_sdwa v93, v74 src0_sel:BYTE_3
	v_cvt_f32_fp8_sdwa v94, v72 src0_sel:BYTE_1
	s_waitcnt lgkmcnt(1)
	v_cndmask_b32_e32 v59, v63, v91, vcc
	v_cndmask_b32_e32 v58, v62, v90, vcc
	v_pk_add_f32 v[90:91], v[50:51], v[58:59] neg_hi:[0,1]
	v_pk_add_f32 v[50:51], v[50:51], v[58:59] neg_lo:[0,1]
	v_cvt_f32_fp8_sdwa v95, v72 src0_sel:BYTE_3
	v_pk_mul_f32 v[62:63], v[90:91], v[50:51] op_sel:[0,0] op_sel_hi:[0,1]
	v_pk_fma_f32 v[62:63], v[90:91], v[50:51], v[62:63] op_sel:[1,1,0] op_sel_hi:[1,0,1] neg_hi:[0,1,0]
	v_pk_add_f32 v[50:51], v[52:53], v[60:61] neg_hi:[0,1]
	v_pk_add_f32 v[52:53], v[52:53], v[60:61] neg_lo:[0,1]
	v_cvt_f32_fp8_sdwa v72, v71 src0_sel:BYTE_1
	v_pk_mul_f32 v[60:61], v[50:51], v[52:53] op_sel:[0,0] op_sel_hi:[0,1]
	v_pk_fma_f32 v[60:61], v[50:51], v[52:53], v[60:61] op_sel:[1,1,0] op_sel_hi:[1,0,1] neg_hi:[0,1,0]
	s_waitcnt lgkmcnt(0)
	v_pk_add_f32 v[50:51], v[54:55], v[88:89] neg_hi:[0,1]
	v_pk_add_f32 v[52:53], v[54:55], v[88:89] neg_lo:[0,1]
	v_pk_add_f32 v[54:55], v[56:57], v[86:87] neg_hi:[0,1]
	v_pk_add_f32 v[86:87], v[56:57], v[86:87] neg_lo:[0,1]
	v_cvt_f32_fp8_sdwa v98, v70 src0_sel:BYTE_1
	v_pk_mul_f32 v[58:59], v[50:51], v[52:53] op_sel:[0,0] op_sel_hi:[0,1]
	v_pk_fma_f32 v[58:59], v[50:51], v[52:53], v[58:59] op_sel:[1,1,0] op_sel_hi:[1,0,1] neg_hi:[0,1,0]
	ds_read2_b64 v[50:53], v92 offset0:10 offset1:11
	v_pk_mul_f32 v[56:57], v[54:55], v[86:87] op_sel:[0,0] op_sel_hi:[0,1]
	v_pk_fma_f32 v[56:57], v[54:55], v[86:87], v[56:57] op_sel:[1,1,0] op_sel_hi:[1,0,1] neg_hi:[0,1,0]
	ds_read2_b64 v[86:89], v92 offset0:8 offset1:9
	s_waitcnt lgkmcnt(1)
	v_pk_add_f32 v[90:91], v[42:43], v[52:53] neg_hi:[0,1]
	v_pk_add_f32 v[42:43], v[42:43], v[52:53] neg_lo:[0,1]
	v_cvt_f32_fp8_sdwa v99, v70 src0_sel:BYTE_3
	v_pk_mul_f32 v[54:55], v[90:91], v[42:43] op_sel:[0,0] op_sel_hi:[0,1]
	v_pk_fma_f32 v[54:55], v[90:91], v[42:43], v[54:55] op_sel:[1,1,0] op_sel_hi:[1,0,1] neg_hi:[0,1,0]
	v_pk_add_f32 v[42:43], v[44:45], v[50:51] neg_hi:[0,1]
	v_pk_add_f32 v[44:45], v[44:45], v[50:51] neg_lo:[0,1]
	s_mov_b32 s6, 0x3f6c835e
	v_pk_mul_f32 v[52:53], v[42:43], v[44:45] op_sel:[0,0] op_sel_hi:[0,1]
	v_pk_fma_f32 v[52:53], v[42:43], v[44:45], v[52:53] op_sel:[1,1,0] op_sel_hi:[1,0,1] neg_hi:[0,1,0]
	s_waitcnt lgkmcnt(0)
	v_pk_add_f32 v[42:43], v[48:49], v[88:89] neg_hi:[0,1]
	v_pk_add_f32 v[44:45], v[48:49], v[88:89] neg_lo:[0,1]
	v_pk_add_f32 v[88:89], v[46:47], v[86:87] neg_hi:[0,1]
	v_pk_add_f32 v[46:47], v[46:47], v[86:87] neg_lo:[0,1]
	s_mov_b32 s7, 0xbec3ef15
	v_pk_mul_f32 v[50:51], v[42:43], v[44:45] op_sel:[0,0] op_sel_hi:[0,1]
	v_pk_fma_f32 v[50:51], v[42:43], v[44:45], v[50:51] op_sel:[1,1,0] op_sel_hi:[1,0,1] neg_hi:[0,1,0]
	ds_read2_b64 v[42:45], v92 offset0:6 offset1:7
	v_pk_mul_f32 v[48:49], v[88:89], v[46:47] op_sel:[0,0] op_sel_hi:[0,1]
	v_pk_fma_f32 v[48:49], v[88:89], v[46:47], v[48:49] op_sel:[1,1,0] op_sel_hi:[1,0,1] neg_hi:[0,1,0]
	ds_read2_b64 v[86:89], v92 offset0:4 offset1:5
	s_waitcnt lgkmcnt(1)
	v_pk_add_f32 v[90:91], v[36:37], v[44:45] neg_hi:[0,1]
	v_pk_add_f32 v[36:37], v[36:37], v[44:45] neg_lo:[0,1]
	s_mov_b32 s9, s8
	v_pk_mul_f32 v[46:47], v[90:91], v[36:37] op_sel:[0,0] op_sel_hi:[0,1]
	v_pk_fma_f32 v[46:47], v[90:91], v[36:37], v[46:47] op_sel:[1,1,0] op_sel_hi:[1,0,1] neg_hi:[0,1,0]
	v_pk_add_f32 v[36:37], v[38:39], v[42:43] neg_hi:[0,1]
	v_pk_add_f32 v[38:39], v[38:39], v[42:43] neg_lo:[0,1]
	v_cvt_f32_fp8_sdwa v90, v76 src0_sel:BYTE_1
	v_pk_mul_f32 v[44:45], v[36:37], v[38:39] op_sel:[0,0] op_sel_hi:[0,1]
	v_pk_fma_f32 v[44:45], v[36:37], v[38:39], v[44:45] op_sel:[1,1,0] op_sel_hi:[1,0,1] neg_hi:[0,1,0]
	s_waitcnt lgkmcnt(0)
	v_pk_add_f32 v[36:37], v[40:41], v[88:89] neg_hi:[0,1]
	v_pk_add_f32 v[38:39], v[40:41], v[88:89] neg_lo:[0,1]
	v_pk_add_f32 v[88:89], v[68:69], v[86:87] neg_hi:[0,1]
	v_pk_add_f32 v[68:69], v[68:69], v[86:87] neg_lo:[0,1]
	v_cvt_f32_fp8_sdwa v91, v76 src0_sel:BYTE_3
	v_pk_mul_f32 v[42:43], v[36:37], v[38:39] op_sel:[0,0] op_sel_hi:[0,1]
	v_pk_fma_f32 v[42:43], v[36:37], v[38:39], v[42:43] op_sel:[1,1,0] op_sel_hi:[1,0,1] neg_hi:[0,1,0]
	ds_read2_b64 v[36:39], v92 offset0:2 offset1:3
	v_pk_mul_f32 v[40:41], v[88:89], v[68:69] op_sel:[0,0] op_sel_hi:[0,1]
	v_pk_fma_f32 v[40:41], v[88:89], v[68:69], v[40:41] op_sel:[1,1,0] op_sel_hi:[1,0,1] neg_hi:[0,1,0]
	ds_read2_b64 v[86:89], v92 offset1:1
	s_waitcnt lgkmcnt(1)
	v_pk_add_f32 v[68:69], v[32:33], v[38:39] neg_hi:[0,1]
	v_pk_add_f32 v[32:33], v[32:33], v[38:39] neg_lo:[0,1]
	v_cvt_f32_fp8_sdwa v76, v75 src0_sel:BYTE_1
	v_pk_mul_f32 v[38:39], v[68:69], v[32:33] op_sel:[0,0] op_sel_hi:[0,1]
	v_pk_fma_f32 v[38:39], v[68:69], v[32:33], v[38:39] op_sel:[1,1,0] op_sel_hi:[1,0,1] neg_hi:[0,1,0]
	v_pk_add_f32 v[32:33], v[34:35], v[36:37] neg_hi:[0,1]
	v_pk_add_f32 v[34:35], v[34:35], v[36:37] neg_lo:[0,1]
	v_cvt_f32_fp8_sdwa v68, v83 src0_sel:BYTE_1
	v_pk_mul_f32 v[36:37], v[32:33], v[34:35] op_sel:[0,0] op_sel_hi:[0,1]
	v_pk_fma_f32 v[36:37], v[32:33], v[34:35], v[36:37] op_sel:[1,1,0] op_sel_hi:[1,0,1] neg_hi:[0,1,0]
	s_waitcnt lgkmcnt(0)
	v_pk_add_f32 v[32:33], v[64:65], v[88:89] neg_hi:[0,1]
	v_pk_add_f32 v[64:65], v[64:65], v[88:89] neg_lo:[0,1]
	v_cvt_f32_fp8_sdwa v69, v83 src0_sel:BYTE_3
	v_pk_mul_f32 v[34:35], v[32:33], v[64:65] op_sel:[0,0] op_sel_hi:[0,1]
	v_pk_fma_f32 v[34:35], v[32:33], v[64:65], v[34:35] op_sel:[1,1,0] op_sel_hi:[1,0,1] neg_hi:[0,1,0]
	v_pk_add_f32 v[64:65], v[66:67], v[86:87] neg_hi:[0,1]
	v_pk_add_f32 v[66:67], v[66:67], v[86:87] neg_lo:[0,1]
	v_cvt_f32_fp8_sdwa v83, v81 src0_sel:BYTE_3
	v_pk_mul_f32 v[32:33], v[64:65], v[66:67] op_sel:[0,0] op_sel_hi:[0,1]
	v_pk_fma_f32 v[32:33], v[64:65], v[66:67], v[32:33] op_sel:[1,1,0] op_sel_hi:[1,0,1] neg_hi:[0,1,0]
	v_cvt_f32_fp8_sdwa v64, v85 src0_sel:BYTE_1
	v_cvt_f32_fp8_sdwa v65, v85 src0_sel:BYTE_3
	v_cvt_f32_fp8_sdwa v66, v84 src0_sel:BYTE_1
	v_cvt_f32_fp8_sdwa v67, v84 src0_sel:BYTE_3
	v_cvt_f32_fp8_sdwa v84, v82 src0_sel:BYTE_1
	v_cvt_f32_fp8_sdwa v85, v82 src0_sel:BYTE_3
	v_cvt_f32_fp8_sdwa v82, v81 src0_sel:BYTE_1
	v_cvt_f32_fp8_sdwa v86, v80 src0_sel:BYTE_1
	v_cvt_f32_fp8_sdwa v87, v80 src0_sel:BYTE_3
	v_cvt_f32_fp8_sdwa v80, v79 src0_sel:BYTE_1
	v_cvt_f32_fp8_sdwa v81, v79 src0_sel:BYTE_3
	v_cvt_f32_fp8_sdwa v88, v78 src0_sel:BYTE_1
	v_cvt_f32_fp8_sdwa v89, v78 src0_sel:BYTE_3
	v_cvt_f32_fp8_sdwa v78, v77 src0_sel:BYTE_1
	v_cvt_f32_fp8_sdwa v79, v77 src0_sel:BYTE_3
	v_cvt_f32_fp8_sdwa v77, v75 src0_sel:BYTE_3
	v_cvt_f32_fp8_sdwa v92, v74 src0_sel:BYTE_1
	v_cvt_f32_fp8_sdwa v74, v73 src0_sel:BYTE_1
	v_cvt_f32_fp8_sdwa v75, v73 src0_sel:BYTE_3
	v_cvt_f32_fp8_sdwa v73, v71 src0_sel:BYTE_3
	v_pk_add_f32 v[70:71], v[64:65], v[78:79]
	v_pk_add_f32 v[64:65], v[64:65], v[78:79] neg_lo:[0,1] neg_hi:[0,1]
	v_pk_add_f32 v[78:79], v[82:83], v[74:75]
	v_pk_add_f32 v[74:75], v[82:83], v[74:75] neg_lo:[0,1] neg_hi:[0,1]
	v_pk_add_f32 v[82:83], v[70:71], v[78:79]
	v_pk_add_f32 v[70:71], v[70:71], v[78:79] neg_lo:[0,1] neg_hi:[0,1]
	v_pk_add_f32 v[78:79], v[64:65], v[74:75] op_sel:[0,1] op_sel_hi:[1,0] neg_hi:[0,1]
	v_pk_add_f32 v[64:65], v[64:65], v[74:75] op_sel:[0,1] op_sel_hi:[1,0] neg_lo:[0,1]
	v_pk_add_f32 v[74:75], v[66:67], v[90:91]
	v_pk_add_f32 v[66:67], v[66:67], v[90:91] neg_lo:[0,1] neg_hi:[0,1]
	v_pk_add_f32 v[90:91], v[86:87], v[94:95]
	v_pk_add_f32 v[86:87], v[86:87], v[94:95] neg_lo:[0,1] neg_hi:[0,1]
	v_pk_add_f32 v[94:95], v[74:75], v[90:91]
	v_pk_add_f32 v[74:75], v[74:75], v[90:91] neg_lo:[0,1] neg_hi:[0,1]
	v_pk_add_f32 v[90:91], v[66:67], v[86:87] op_sel:[0,1] op_sel_hi:[1,0] neg_hi:[0,1]
	v_pk_add_f32 v[66:67], v[66:67], v[86:87] op_sel:[0,1] op_sel_hi:[1,0] neg_lo:[0,1]
	v_pk_add_f32 v[86:87], v[68:69], v[76:77]
	v_pk_add_f32 v[68:69], v[68:69], v[76:77] neg_lo:[0,1] neg_hi:[0,1]
	v_pk_add_f32 v[76:77], v[80:81], v[72:73]
	v_pk_add_f32 v[72:73], v[80:81], v[72:73] neg_lo:[0,1] neg_hi:[0,1]
	v_pk_add_f32 v[80:81], v[86:87], v[76:77]
	v_pk_add_f32 v[76:77], v[86:87], v[76:77] neg_lo:[0,1] neg_hi:[0,1]
	v_pk_add_f32 v[86:87], v[68:69], v[72:73] op_sel:[0,1] op_sel_hi:[1,0] neg_hi:[0,1]
	v_pk_add_f32 v[68:69], v[68:69], v[72:73] op_sel:[0,1] op_sel_hi:[1,0] neg_lo:[0,1]
	v_pk_add_f32 v[72:73], v[84:85], v[92:93]
	v_pk_add_f32 v[84:85], v[84:85], v[92:93] neg_lo:[0,1] neg_hi:[0,1]
	v_pk_add_f32 v[92:93], v[88:89], v[98:99]
	v_pk_add_f32 v[88:89], v[88:89], v[98:99] neg_lo:[0,1] neg_hi:[0,1]
	v_pk_add_f32 v[98:99], v[72:73], v[92:93]
	v_pk_add_f32 v[72:73], v[72:73], v[92:93] neg_lo:[0,1] neg_hi:[0,1]
	v_pk_add_f32 v[92:93], v[84:85], v[88:89] op_sel:[0,1] op_sel_hi:[1,0] neg_hi:[0,1]
	v_pk_add_f32 v[84:85], v[84:85], v[88:89] op_sel:[0,1] op_sel_hi:[1,0] neg_lo:[0,1]
	v_pk_mul_f32 v[88:89], v[90:91], s[6:7] op_sel:[0,0] op_sel_hi:[0,1]
	v_pk_fma_f32 v[88:89], v[90:91], s[6:7], v[88:89] op_sel:[1,1,0] op_sel_hi:[1,0,1] neg_lo:[0,1,0]
	v_pk_mul_f32 v[90:91], v[66:67], s[10:11] op_sel:[0,0] op_sel_hi:[0,1]
	v_pk_fma_f32 v[90:91], v[66:67], s[10:11], v[90:91] op_sel:[1,1,0] op_sel_hi:[1,0,1] neg_lo:[0,1,0]
	v_pk_add_f32 v[66:67], v[86:87], v[86:87] op_sel:[0,1] op_sel_hi:[1,0] neg_hi:[0,1]
	s_nop 0
	v_pk_add_f32 v[72:73], v[72:73], v[72:73] op_sel:[0,1] op_sel_hi:[1,0] neg_lo:[0,1]
	v_pk_mul_f32 v[86:87], v[92:93], s[10:11] op_sel:[0,0] op_sel_hi:[0,1]
	v_pk_fma_f32 v[86:87], v[92:93], s[10:11], v[86:87] op_sel:[1,1,0] op_sel_hi:[1,0,1] neg_lo:[0,1,0]
	s_mov_b32 s14, s11
	v_pk_mul_f32 v[66:67], v[66:67], s[8:9]
	s_mov_b32 s15, s10
	v_pk_mul_f32 v[92:93], v[84:85], s[14:15] op_sel:[0,0] op_sel_hi:[0,1]
	v_pk_fma_f32 v[92:93], v[84:85], s[14:15], v[92:93] op_sel:[1,1,0] op_sel_hi:[1,0,1] neg_lo:[0,1,0]
	v_pk_add_f32 v[84:85], v[82:83], v[80:81]
	v_pk_add_f32 v[80:81], v[82:83], v[80:81] neg_lo:[0,1] neg_hi:[0,1]
	v_pk_add_f32 v[82:83], v[94:95], v[98:99]
	v_pk_add_f32 v[94:95], v[94:95], v[98:99] neg_lo:[0,1] neg_hi:[0,1]
	v_pk_add_f32 v[74:75], v[74:75], v[74:75] op_sel:[0,1] op_sel_hi:[1,0] neg_hi:[0,1]
	v_pk_add_f32 v[68:69], v[68:69], v[68:69] op_sel:[0,1] op_sel_hi:[1,0] neg_lo:[0,1]
	s_mov_b32 s13, s12
	v_pk_mul_f32 v[72:73], v[72:73], s[12:13]
	v_pk_add_f32 v[98:99], v[84:85], v[82:83]
	v_pk_add_f32 v[82:83], v[84:85], v[82:83] neg_lo:[0,1] neg_hi:[0,1]
	v_pk_add_f32 v[84:85], v[80:81], v[94:95] op_sel:[0,1] op_sel_hi:[1,0] neg_hi:[0,1]
	v_pk_add_f32 v[80:81], v[80:81], v[94:95] op_sel:[0,1] op_sel_hi:[1,0] neg_lo:[0,1]
	v_pk_add_f32 v[94:95], v[78:79], v[66:67]
	v_pk_add_f32 v[66:67], v[78:79], v[66:67] neg_lo:[0,1] neg_hi:[0,1]
	v_pk_add_f32 v[78:79], v[88:89], v[86:87]
	v_pk_add_f32 v[86:87], v[88:89], v[86:87] neg_lo:[0,1] neg_hi:[0,1]
	v_pk_mul_f32 v[74:75], v[74:75], s[8:9]
	v_pk_mul_f32 v[68:69], v[68:69], s[12:13]
	v_pk_add_f32 v[88:89], v[94:95], v[78:79]
	v_pk_add_f32 v[78:79], v[94:95], v[78:79] neg_lo:[0,1] neg_hi:[0,1]
	v_pk_add_f32 v[94:95], v[66:67], v[86:87] op_sel:[0,1] op_sel_hi:[1,0] neg_hi:[0,1]
	v_pk_add_f32 v[66:67], v[66:67], v[86:87] op_sel:[0,1] op_sel_hi:[1,0] neg_lo:[0,1]
	v_pk_add_f32 v[86:87], v[70:71], v[76:77] op_sel:[0,1] op_sel_hi:[1,0] neg_hi:[0,1]
	v_pk_add_f32 v[70:71], v[70:71], v[76:77] op_sel:[0,1] op_sel_hi:[1,0] neg_lo:[0,1]
	v_pk_add_f32 v[76:77], v[74:75], v[72:73]
	v_pk_add_f32 v[72:73], v[74:75], v[72:73] neg_lo:[0,1] neg_hi:[0,1]
	v_pk_add_f32 v[74:75], v[76:77], v[86:87]
	v_pk_add_f32 v[76:77], v[86:87], v[76:77] neg_lo:[0,1] neg_hi:[0,1]
	v_pk_add_f32 v[86:87], v[70:71], v[72:73] op_sel:[0,1] op_sel_hi:[1,0] neg_hi:[0,1]
	v_pk_add_f32 v[70:71], v[70:71], v[72:73] op_sel:[0,1] op_sel_hi:[1,0] neg_lo:[0,1]
	v_pk_add_f32 v[72:73], v[64:65], v[68:69]
	v_pk_add_f32 v[64:65], v[64:65], v[68:69] neg_lo:[0,1] neg_hi:[0,1]
	v_pk_add_f32 v[68:69], v[90:91], v[92:93]
	v_pk_add_f32 v[90:91], v[90:91], v[92:93] neg_lo:[0,1] neg_hi:[0,1]
	v_pk_add_f32 v[92:93], v[72:73], v[68:69]
	v_pk_add_f32 v[68:69], v[72:73], v[68:69] neg_lo:[0,1] neg_hi:[0,1]
	v_pk_add_f32 v[72:73], v[64:65], v[90:91] op_sel:[0,1] op_sel_hi:[1,0] neg_hi:[0,1]
	v_pk_add_f32 v[64:65], v[64:65], v[90:91] op_sel:[0,1] op_sel_hi:[1,0] neg_lo:[0,1]
	v_pk_mul_f32 v[90:91], v[88:89], v[30:31] op_sel:[0,0] op_sel_hi:[0,1]
	v_pk_fma_f32 v[90:91], v[88:89], v[30:31], v[90:91] op_sel:[1,1,0] op_sel_hi:[1,0,1] neg_lo:[0,1,0]
	v_pk_mul_f32 v[88:89], v[74:75], v[28:29] op_sel:[0,0] op_sel_hi:[0,1]
	v_pk_fma_f32 v[88:89], v[74:75], v[28:29], v[88:89] op_sel:[1,1,0] op_sel_hi:[1,0,1] neg_lo:[0,1,0]
	v_pk_mul_f32 v[74:75], v[92:93], v[26:27] op_sel:[0,0] op_sel_hi:[0,1]
	v_pk_fma_f32 v[74:75], v[92:93], v[26:27], v[74:75] op_sel:[1,1,0] op_sel_hi:[1,0,1] neg_lo:[0,1,0]
	s_barrier
	ds_write_b64 v1, v[74:75] offset:6552
	v_pk_mul_f32 v[74:75], v[84:85], v[24:25] op_sel:[0,0] op_sel_hi:[0,1]
	v_pk_fma_f32 v[74:75], v[84:85], v[24:25], v[74:75] op_sel:[1,1,0] op_sel_hi:[1,0,1] neg_lo:[0,1,0]
	ds_write_b64 v1, v[74:75] offset:8736
	v_pk_mul_f32 v[74:75], v[94:95], v[20:21] op_sel:[0,0] op_sel_hi:[0,1]
	v_pk_fma_f32 v[74:75], v[94:95], v[20:21], v[74:75] op_sel:[1,1,0] op_sel_hi:[1,0,1] neg_lo:[0,1,0]
	ds_write_b64 v1, v[74:75] offset:10920
	v_pk_mul_f32 v[74:75], v[86:87], v[16:17] op_sel:[0,0] op_sel_hi:[0,1]
	v_pk_fma_f32 v[74:75], v[86:87], v[16:17], v[74:75] op_sel:[1,1,0] op_sel_hi:[1,0,1] neg_lo:[0,1,0]
	ds_write_b64 v1, v[74:75] offset:13104
	v_pk_mul_f32 v[74:75], v[72:73], v[10:11] op_sel:[0,0] op_sel_hi:[0,1]
	v_pk_fma_f32 v[74:75], v[72:73], v[10:11], v[74:75] op_sel:[1,1,0] op_sel_hi:[1,0,1] neg_lo:[0,1,0]
	v_pk_mul_f32 v[72:73], v[82:83], v[22:23] op_sel:[0,0] op_sel_hi:[0,1]
	v_pk_fma_f32 v[72:73], v[82:83], v[22:23], v[72:73] op_sel:[1,1,0] op_sel_hi:[1,0,1] neg_lo:[0,1,0]
	ds_write_b64 v1, v[72:73] offset:17472
	v_pk_mul_f32 v[72:73], v[78:79], v[18:19] op_sel:[0,0] op_sel_hi:[0,1]
	v_pk_fma_f32 v[72:73], v[78:79], v[18:19], v[72:73] op_sel:[1,1,0] op_sel_hi:[1,0,1] neg_lo:[0,1,0]
	ds_write_b64 v1, v[72:73] offset:19656
	v_pk_mul_f32 v[72:73], v[76:77], v[12:13] op_sel:[0,0] op_sel_hi:[0,1]
	v_pk_fma_f32 v[72:73], v[76:77], v[12:13], v[72:73] op_sel:[1,1,0] op_sel_hi:[1,0,1] neg_lo:[0,1,0]
	ds_write_b64 v1, v[72:73] offset:21840
	v_pk_mul_f32 v[72:73], v[68:69], v[14:15] op_sel:[0,0] op_sel_hi:[0,1]
	v_pk_fma_f32 v[72:73], v[68:69], v[14:15], v[72:73] op_sel:[1,1,0] op_sel_hi:[1,0,1] neg_lo:[0,1,0]
	v_pk_mul_f32 v[68:69], v[80:81], v[6:7] op_sel:[0,0] op_sel_hi:[0,1]
	v_pk_fma_f32 v[68:69], v[80:81], v[6:7], v[68:69] op_sel:[1,1,0] op_sel_hi:[1,0,1] neg_lo:[0,1,0]
	ds_write_b64 v1, v[68:69] offset:26208
	v_pk_mul_f32 v[68:69], v[66:67], v[8:9] op_sel:[0,0] op_sel_hi:[0,1]
	v_pk_fma_f32 v[68:69], v[66:67], v[8:9], v[68:69] op_sel:[1,1,0] op_sel_hi:[1,0,1] neg_lo:[0,1,0]
	v_pk_mul_f32 v[66:67], v[70:71], v[4:5] op_sel:[0,0] op_sel_hi:[0,1]
	v_pk_fma_f32 v[66:67], v[70:71], v[4:5], v[66:67] op_sel:[1,1,0] op_sel_hi:[1,0,1] neg_lo:[0,1,0]
	ds_write_b64 v1, v[66:67] offset:30576
	v_pk_mul_f32 v[66:67], v[64:65], v[2:3] op_sel:[0,0] op_sel_hi:[0,1]
	v_pk_fma_f32 v[66:67], v[64:65], v[2:3], v[66:67] op_sel:[1,1,0] op_sel_hi:[1,0,1] neg_lo:[0,1,0]
	ds_write_b64 v1, v[98:99]
	ds_write_b64 v1, v[90:91] offset:2184
	ds_write_b64 v1, v[88:89] offset:4368
	ds_write_b64 v1, v[74:75] offset:15288
	ds_write_b64 v1, v[72:73] offset:24024
	ds_write_b64 v1, v[68:69] offset:28392
	ds_write_b64 v1, v[66:67] offset:32760
	s_waitcnt lgkmcnt(0)
	s_barrier
	ds_read2_b64 v[64:67], v96 offset1:16
	ds_read2_b64 v[68:71], v96 offset0:32 offset1:48
	ds_read2_b64 v[72:75], v96 offset0:64 offset1:80
	ds_read2_b64 v[76:79], v96 offset0:128 offset1:144
	ds_read2_b64 v[80:83], v96 offset0:96 offset1:112
	ds_read2_b64 v[84:87], v96 offset0:192 offset1:208
	ds_read2_b64 v[88:91], v96 offset0:160 offset1:176
	ds_read2_b64 v[92:95], v96 offset0:224 offset1:240
	s_waitcnt lgkmcnt(4)
	v_pk_add_f32 v[98:99], v[64:65], v[76:77]
	v_pk_add_f32 v[64:65], v[64:65], v[76:77] neg_lo:[0,1] neg_hi:[0,1]
	s_waitcnt lgkmcnt(2)
	v_pk_add_f32 v[76:77], v[72:73], v[84:85]
	v_pk_add_f32 v[72:73], v[72:73], v[84:85] neg_lo:[0,1] neg_hi:[0,1]
	v_pk_add_f32 v[84:85], v[98:99], v[76:77]
	v_pk_add_f32 v[76:77], v[98:99], v[76:77] neg_lo:[0,1] neg_hi:[0,1]
	v_pk_add_f32 v[98:99], v[64:65], v[72:73] op_sel:[0,1] op_sel_hi:[1,0] neg_hi:[0,1]
	v_pk_add_f32 v[64:65], v[64:65], v[72:73] op_sel:[0,1] op_sel_hi:[1,0] neg_lo:[0,1]
	v_pk_add_f32 v[72:73], v[66:67], v[78:79]
	v_pk_add_f32 v[66:67], v[66:67], v[78:79] neg_lo:[0,1] neg_hi:[0,1]
	v_pk_add_f32 v[78:79], v[74:75], v[86:87]
	v_pk_add_f32 v[74:75], v[74:75], v[86:87] neg_lo:[0,1] neg_hi:[0,1]
	v_pk_add_f32 v[86:87], v[72:73], v[78:79]
	v_pk_add_f32 v[72:73], v[72:73], v[78:79] neg_lo:[0,1] neg_hi:[0,1]
	v_pk_add_f32 v[78:79], v[66:67], v[74:75] op_sel:[0,1] op_sel_hi:[1,0] neg_hi:[0,1]
	v_pk_add_f32 v[66:67], v[66:67], v[74:75] op_sel:[0,1] op_sel_hi:[1,0] neg_lo:[0,1]
	s_waitcnt lgkmcnt(1)
	v_pk_add_f32 v[74:75], v[68:69], v[88:89]
	v_pk_add_f32 v[68:69], v[68:69], v[88:89] neg_lo:[0,1] neg_hi:[0,1]
	s_waitcnt lgkmcnt(0)
	v_pk_add_f32 v[88:89], v[80:81], v[92:93]
	v_pk_add_f32 v[80:81], v[80:81], v[92:93] neg_lo:[0,1] neg_hi:[0,1]
	v_pk_add_f32 v[92:93], v[74:75], v[88:89]
	v_pk_add_f32 v[74:75], v[74:75], v[88:89] neg_lo:[0,1] neg_hi:[0,1]
	v_pk_add_f32 v[88:89], v[68:69], v[80:81] op_sel:[0,1] op_sel_hi:[1,0] neg_hi:[0,1]
	v_pk_add_f32 v[68:69], v[68:69], v[80:81] op_sel:[0,1] op_sel_hi:[1,0] neg_lo:[0,1]
	v_pk_add_f32 v[80:81], v[70:71], v[90:91]
	v_pk_add_f32 v[70:71], v[70:71], v[90:91] neg_lo:[0,1] neg_hi:[0,1]
	v_pk_add_f32 v[90:91], v[82:83], v[94:95]
	v_pk_add_f32 v[82:83], v[82:83], v[94:95] neg_lo:[0,1] neg_hi:[0,1]
	v_pk_add_f32 v[94:95], v[80:81], v[90:91]
	v_pk_add_f32 v[80:81], v[80:81], v[90:91] neg_lo:[0,1] neg_hi:[0,1]
	v_pk_add_f32 v[90:91], v[70:71], v[82:83] op_sel:[0,1] op_sel_hi:[1,0] neg_hi:[0,1]
	v_pk_add_f32 v[70:71], v[70:71], v[82:83] op_sel:[0,1] op_sel_hi:[1,0] neg_lo:[0,1]
	v_pk_mul_f32 v[82:83], v[78:79], s[6:7] op_sel:[0,0] op_sel_hi:[0,1]
	v_pk_fma_f32 v[82:83], v[78:79], s[6:7], v[82:83] op_sel:[1,1,0] op_sel_hi:[1,0,1] neg_lo:[0,1,0]
	v_pk_mul_f32 v[78:79], v[66:67], s[10:11] op_sel:[0,0] op_sel_hi:[0,1]
	v_pk_fma_f32 v[78:79], v[66:67], s[10:11], v[78:79] op_sel:[1,1,0] op_sel_hi:[1,0,1] neg_lo:[0,1,0]
	v_pk_add_f32 v[66:67], v[88:89], v[88:89] op_sel:[0,1] op_sel_hi:[1,0] neg_hi:[0,1]
	v_pk_add_f32 v[72:73], v[72:73], v[72:73] op_sel:[0,1] op_sel_hi:[1,0] neg_hi:[0,1]
	s_nop 0
	v_pk_mul_f32 v[88:89], v[90:91], s[10:11] op_sel:[0,0] op_sel_hi:[0,1]
	v_pk_fma_f32 v[88:89], v[90:91], s[10:11], v[88:89] op_sel:[1,1,0] op_sel_hi:[1,0,1] neg_lo:[0,1,0]
	v_pk_mul_f32 v[90:91], v[70:71], s[14:15] op_sel:[0,0] op_sel_hi:[0,1]
	v_pk_fma_f32 v[90:91], v[70:71], s[14:15], v[90:91] op_sel:[1,1,0] op_sel_hi:[1,0,1] neg_lo:[0,1,0]
	v_pk_add_f32 v[70:71], v[84:85], v[92:93]
	v_pk_mul_f32 v[66:67], v[66:67], s[8:9]
	v_pk_add_f32 v[84:85], v[84:85], v[92:93] neg_lo:[0,1] neg_hi:[0,1]
	v_pk_add_f32 v[92:93], v[86:87], v[94:95]
	v_pk_add_f32 v[86:87], v[86:87], v[94:95] neg_lo:[0,1] neg_hi:[0,1]
	v_pk_add_f32 v[68:69], v[68:69], v[68:69] op_sel:[0,1] op_sel_hi:[1,0] neg_lo:[0,1]
	v_pk_add_f32 v[80:81], v[80:81], v[80:81] op_sel:[0,1] op_sel_hi:[1,0] neg_lo:[0,1]
	v_pk_add_f32 v[94:95], v[70:71], v[92:93]
	v_pk_add_f32 v[92:93], v[70:71], v[92:93] neg_lo:[0,1] neg_hi:[0,1]
	v_pk_add_f32 v[100:101], v[84:85], v[86:87] op_sel:[0,1] op_sel_hi:[1,0] neg_hi:[0,1]
	v_pk_add_f32 v[84:85], v[84:85], v[86:87] op_sel:[0,1] op_sel_hi:[1,0] neg_lo:[0,1]
	v_pk_add_f32 v[70:71], v[98:99], v[66:67]
	v_pk_add_f32 v[66:67], v[98:99], v[66:67] neg_lo:[0,1] neg_hi:[0,1]
	v_pk_add_f32 v[86:87], v[82:83], v[88:89]
	v_pk_add_f32 v[82:83], v[82:83], v[88:89] neg_lo:[0,1] neg_hi:[0,1]
	v_pk_mul_f32 v[72:73], v[72:73], s[8:9]
	v_pk_mul_f32 v[68:69], v[68:69], s[12:13]
	v_pk_mul_f32 v[80:81], v[80:81], s[12:13]
	v_pk_add_f32 v[88:89], v[70:71], v[86:87]
	v_pk_add_f32 v[86:87], v[70:71], v[86:87] neg_lo:[0,1] neg_hi:[0,1]
	v_pk_add_f32 v[98:99], v[66:67], v[82:83] op_sel:[0,1] op_sel_hi:[1,0] neg_hi:[0,1]
	v_pk_add_f32 v[82:83], v[66:67], v[82:83] op_sel:[0,1] op_sel_hi:[1,0] neg_lo:[0,1]
	v_pk_add_f32 v[66:67], v[76:77], v[74:75] op_sel:[0,1] op_sel_hi:[1,0] neg_hi:[0,1]
	v_pk_add_f32 v[70:71], v[76:77], v[74:75] op_sel:[0,1] op_sel_hi:[1,0] neg_lo:[0,1]
	v_pk_add_f32 v[74:75], v[72:73], v[80:81]
	v_pk_add_f32 v[72:73], v[72:73], v[80:81] neg_lo:[0,1] neg_hi:[0,1]
	v_pk_add_f32 v[76:77], v[74:75], v[66:67]
	v_pk_add_f32 v[74:75], v[66:67], v[74:75] neg_lo:[0,1] neg_hi:[0,1]
	v_pk_add_f32 v[66:67], v[64:65], v[68:69]
	v_pk_add_f32 v[64:65], v[64:65], v[68:69] neg_lo:[0,1] neg_hi:[0,1]
	v_pk_add_f32 v[68:69], v[78:79], v[90:91]
	v_pk_add_f32 v[80:81], v[70:71], v[72:73] op_sel:[0,1] op_sel_hi:[1,0] neg_hi:[0,1]
	v_pk_add_f32 v[72:73], v[70:71], v[72:73] op_sel:[0,1] op_sel_hi:[1,0] neg_lo:[0,1]
	v_pk_add_f32 v[70:71], v[78:79], v[90:91] neg_lo:[0,1] neg_hi:[0,1]
	v_pk_add_f32 v[78:79], v[66:67], v[68:69]
	v_pk_add_f32 v[90:91], v[66:67], v[68:69] neg_lo:[0,1] neg_hi:[0,1]
	v_mov_b32_e32 v68, v0
	v_pk_add_f32 v[102:103], v[64:65], v[70:71] op_sel:[0,1] op_sel_hi:[1,0] neg_hi:[0,1]
	v_pk_add_f32 v[104:105], v[64:65], v[70:71] op_sel:[0,1] op_sel_hi:[1,0] neg_lo:[0,1]
	s_nop 0
	v_ashrrev_i32_e32 v64, 4, v68
	v_lshlrev_b32_e32 v97, 3, v64
	v_add_u32_e32 v108, 0x8800, v97
	v_and_b32_e32 v68, 15, v68
	ds_read2_b64 v[64:67], v108 offset0:16 offset1:32
	v_mad_u32_u24 v109, v68, s5, v97
	ds_read2_b64 v[68:71], v108 offset0:48 offset1:64
	s_waitcnt lgkmcnt(1)
	v_pk_mul_f32 v[106:107], v[88:89], v[64:65] op_sel:[0,0] op_sel_hi:[0,1]
	v_pk_fma_f32 v[106:107], v[88:89], v[64:65], v[106:107] op_sel:[1,1,0] op_sel_hi:[1,0,1] neg_lo:[0,1,0]
	v_pk_mul_f32 v[88:89], v[76:77], v[66:67] op_sel:[0,0] op_sel_hi:[0,1]
	v_pk_fma_f32 v[88:89], v[76:77], v[66:67], v[88:89] op_sel:[1,1,0] op_sel_hi:[1,0,1] neg_lo:[0,1,0]
	s_waitcnt lgkmcnt(0)
	v_pk_mul_f32 v[76:77], v[78:79], v[68:69] op_sel:[0,0] op_sel_hi:[0,1]
	v_pk_fma_f32 v[76:77], v[78:79], v[68:69], v[76:77] op_sel:[1,1,0] op_sel_hi:[1,0,1] neg_lo:[0,1,0]
	ds_write2_b64 v109, v[88:89], v[76:77] offset0:32 offset1:48
	v_pk_mul_f32 v[76:77], v[100:101], v[70:71] op_sel:[0,0] op_sel_hi:[0,1]
	v_pk_fma_f32 v[76:77], v[100:101], v[70:71], v[76:77] op_sel:[1,1,0] op_sel_hi:[1,0,1] neg_lo:[0,1,0]
	ds_read2_b64 v[64:67], v108 offset0:80 offset1:96
	s_waitcnt lgkmcnt(0)
	v_pk_mul_f32 v[78:79], v[98:99], v[64:65] op_sel:[0,0] op_sel_hi:[0,1]
	v_pk_fma_f32 v[78:79], v[98:99], v[64:65], v[78:79] op_sel:[1,1,0] op_sel_hi:[1,0,1] neg_lo:[0,1,0]
	ds_write2_b64 v109, v[76:77], v[78:79] offset0:64 offset1:80
	v_pk_mul_f32 v[76:77], v[80:81], v[66:67] op_sel:[0,0] op_sel_hi:[0,1]
	v_pk_fma_f32 v[76:77], v[80:81], v[66:67], v[76:77] op_sel:[1,1,0] op_sel_hi:[1,0,1] neg_lo:[0,1,0]
	ds_read2_b64 v[68:71], v108 offset0:112 offset1:128
	ds_read2_b64 v[64:67], v108 offset0:144 offset1:160
	s_waitcnt lgkmcnt(1)
	v_pk_mul_f32 v[78:79], v[102:103], v[68:69] op_sel:[0,0] op_sel_hi:[0,1]
	v_pk_fma_f32 v[78:79], v[102:103], v[68:69], v[78:79] op_sel:[1,1,0] op_sel_hi:[1,0,1] neg_lo:[0,1,0]
	ds_write2_b64 v109, v[76:77], v[78:79] offset0:96 offset1:112
	v_pk_mul_f32 v[76:77], v[92:93], v[70:71] op_sel:[0,0] op_sel_hi:[0,1]
	v_pk_fma_f32 v[76:77], v[92:93], v[70:71], v[76:77] op_sel:[1,1,0] op_sel_hi:[1,0,1] neg_lo:[0,1,0]
	ds_read2_b64 v[68:71], v108 offset0:176 offset1:192
	s_waitcnt lgkmcnt(2)
	v_pk_mul_f32 v[78:79], v[86:87], v[64:65] op_sel:[0,0] op_sel_hi:[0,1]
	v_pk_fma_f32 v[78:79], v[86:87], v[64:65], v[78:79] op_sel:[1,1,0] op_sel_hi:[1,0,1] neg_lo:[0,1,0]
	ds_write2_b64 v109, v[76:77], v[78:79] offset0:128 offset1:144
	v_pk_mul_f32 v[76:77], v[74:75], v[66:67] op_sel:[0,0] op_sel_hi:[0,1]
	v_pk_fma_f32 v[76:77], v[74:75], v[66:67], v[76:77] op_sel:[1,1,0] op_sel_hi:[1,0,1] neg_lo:[0,1,0]
	ds_read2_b64 v[64:67], v108 offset0:208 offset1:224
	s_waitcnt lgkmcnt(2)
	v_pk_mul_f32 v[74:75], v[90:91], v[68:69] op_sel:[0,0] op_sel_hi:[0,1]
	v_pk_fma_f32 v[74:75], v[90:91], v[68:69], v[74:75] op_sel:[1,1,0] op_sel_hi:[1,0,1] neg_lo:[0,1,0]
	ds_write2_b64 v109, v[76:77], v[74:75] offset0:160 offset1:176
	v_pk_mul_f32 v[74:75], v[84:85], v[70:71] op_sel:[0,0] op_sel_hi:[0,1]
	v_pk_fma_f32 v[74:75], v[84:85], v[70:71], v[74:75] op_sel:[1,1,0] op_sel_hi:[1,0,1] neg_lo:[0,1,0]
	s_waitcnt lgkmcnt(1)
	v_pk_mul_f32 v[70:71], v[82:83], v[64:65] op_sel:[0,0] op_sel_hi:[0,1]
	v_pk_fma_f32 v[70:71], v[82:83], v[64:65], v[70:71] op_sel:[1,1,0] op_sel_hi:[1,0,1] neg_lo:[0,1,0]
	v_pk_mul_f32 v[64:65], v[72:73], v[66:67] op_sel:[0,0] op_sel_hi:[0,1]
	v_pk_fma_f32 v[64:65], v[72:73], v[66:67], v[64:65] op_sel:[1,1,0] op_sel_hi:[1,0,1] neg_lo:[0,1,0]
	ds_read_b64 v[68:69], v97 offset:36736
	s_waitcnt lgkmcnt(0)
	v_pk_mul_f32 v[66:67], v[104:105], v[68:69] op_sel:[0,0] op_sel_hi:[0,1]
	v_pk_fma_f32 v[66:67], v[104:105], v[68:69], v[66:67] op_sel:[1,1,0] op_sel_hi:[1,0,1] neg_lo:[0,1,0]
	ds_write2_b64 v109, v[64:65], v[66:67] offset0:224 offset1:240
	v_mov_b32_e32 v64, v0
	ds_write2_b64 v109, v[94:95], v[106:107] offset1:16
	ds_write2_b64 v109, v[74:75], v[70:71] offset0:192 offset1:208
	s_waitcnt lgkmcnt(0)
	s_barrier
	s_nop 0
	v_and_b32_e32 v65, 15, v64
	v_and_b32_e32 v64, 0x1ffffff0, v64
	v_lshlrev_b32_e32 v64, 3, v64
	v_mad_u32_u24 v92, v65, s5, v64
	ds_read2_b64 v[64:67], v92 offset1:1
	ds_read2_b64 v[68:71], v92 offset0:2 offset1:3
	ds_read2_b64 v[72:75], v92 offset0:8 offset1:9
	ds_read2_b64 v[76:79], v92 offset0:4 offset1:5
	ds_read2_b64 v[80:83], v92 offset0:6 offset1:7
	ds_read2_b64 v[84:87], v92 offset0:12 offset1:13
	ds_read2_b64 v[88:91], v92 offset0:10 offset1:11
	ds_read2_b64 v[92:95], v92 offset0:14 offset1:15
	s_waitcnt lgkmcnt(5)
	v_pk_add_f32 v[98:99], v[64:65], v[72:73]
	v_pk_add_f32 v[64:65], v[64:65], v[72:73] neg_lo:[0,1] neg_hi:[0,1]
	s_waitcnt lgkmcnt(2)
	v_pk_add_f32 v[72:73], v[76:77], v[84:85]
	v_pk_add_f32 v[76:77], v[76:77], v[84:85] neg_lo:[0,1] neg_hi:[0,1]
	v_pk_add_f32 v[84:85], v[98:99], v[72:73]
	v_pk_add_f32 v[98:99], v[98:99], v[72:73] neg_lo:[0,1] neg_hi:[0,1]
	v_pk_add_f32 v[100:101], v[64:65], v[76:77] op_sel:[0,1] op_sel_hi:[1,0] neg_hi:[0,1]
	v_pk_add_f32 v[102:103], v[64:65], v[76:77] op_sel:[0,1] op_sel_hi:[1,0] neg_lo:[0,1]
	v_pk_add_f32 v[64:65], v[66:67], v[74:75]
	v_pk_add_f32 v[72:73], v[78:79], v[86:87]
	v_pk_add_f32 v[66:67], v[66:67], v[74:75] neg_lo:[0,1] neg_hi:[0,1]
	v_pk_add_f32 v[74:75], v[78:79], v[86:87] neg_lo:[0,1] neg_hi:[0,1]
	v_pk_add_f32 v[76:77], v[64:65], v[72:73]
	v_pk_add_f32 v[64:65], v[64:65], v[72:73] neg_lo:[0,1] neg_hi:[0,1]
	v_pk_add_f32 v[72:73], v[66:67], v[74:75] op_sel:[0,1] op_sel_hi:[1,0] neg_hi:[0,1]
	v_pk_add_f32 v[66:67], v[66:67], v[74:75] op_sel:[0,1] op_sel_hi:[1,0] neg_lo:[0,1]
	s_waitcnt lgkmcnt(1)
	v_pk_add_f32 v[74:75], v[68:69], v[88:89]
	s_waitcnt lgkmcnt(0)
	v_pk_add_f32 v[78:79], v[80:81], v[92:93]
	v_pk_add_f32 v[64:65], v[64:65], v[64:65] op_sel:[0,1] op_sel_hi:[1,0] neg_hi:[0,1]
	v_pk_add_f32 v[68:69], v[68:69], v[88:89] neg_lo:[0,1] neg_hi:[0,1]
	v_pk_add_f32 v[80:81], v[80:81], v[92:93] neg_lo:[0,1] neg_hi:[0,1]
	v_pk_add_f32 v[86:87], v[74:75], v[78:79]
	v_pk_add_f32 v[78:79], v[74:75], v[78:79] neg_lo:[0,1] neg_hi:[0,1]
	v_pk_add_f32 v[74:75], v[68:69], v[80:81] op_sel:[0,1] op_sel_hi:[1,0] neg_hi:[0,1]
	v_pk_mul_f32 v[92:93], v[64:65], s[8:9]
	v_pk_add_f32 v[68:69], v[68:69], v[80:81] op_sel:[0,1] op_sel_hi:[1,0] neg_lo:[0,1]
	v_pk_add_f32 v[80:81], v[70:71], v[90:91]
	v_pk_add_f32 v[64:65], v[74:75], v[74:75] op_sel:[0,1] op_sel_hi:[1,0] neg_hi:[0,1]
	v_pk_add_f32 v[70:71], v[70:71], v[90:91] neg_lo:[0,1] neg_hi:[0,1]
	v_pk_add_f32 v[88:89], v[82:83], v[94:95]
	v_pk_add_f32 v[82:83], v[82:83], v[94:95] neg_lo:[0,1] neg_hi:[0,1]
	v_pk_mul_f32 v[94:95], v[66:67], s[10:11] op_sel:[0,0] op_sel_hi:[0,1]
	v_pk_fma_f32 v[94:95], v[66:67], s[10:11], v[94:95] op_sel:[1,1,0] op_sel_hi:[1,0,1] neg_lo:[0,1,0]
	v_pk_mul_f32 v[66:67], v[64:65], s[8:9]
	v_pk_add_f32 v[64:65], v[68:69], v[68:69] op_sel:[0,1] op_sel_hi:[1,0] neg_lo:[0,1]
	v_pk_add_f32 v[90:91], v[80:81], v[88:89]
	v_pk_add_f32 v[80:81], v[80:81], v[88:89] neg_lo:[0,1] neg_hi:[0,1]
	v_pk_add_f32 v[88:89], v[70:71], v[82:83] op_sel:[0,1] op_sel_hi:[1,0] neg_hi:[0,1]
	v_pk_add_f32 v[70:71], v[70:71], v[82:83] op_sel:[0,1] op_sel_hi:[1,0] neg_lo:[0,1]
	v_pk_mul_f32 v[104:105], v[64:65], s[12:13]
	v_pk_mul_f32 v[82:83], v[72:73], s[6:7] op_sel:[0,0] op_sel_hi:[0,1]
	v_pk_fma_f32 v[82:83], v[72:73], s[6:7], v[82:83] op_sel:[1,1,0] op_sel_hi:[1,0,1] neg_lo:[0,1,0]
	v_pk_add_f32 v[72:73], v[76:77], v[90:91]
	v_pk_add_f32 v[64:65], v[80:81], v[80:81] op_sel:[0,1] op_sel_hi:[1,0] neg_lo:[0,1]
	v_pk_mul_f32 v[68:69], v[88:89], s[10:11] op_sel:[0,0] op_sel_hi:[0,1]
	v_pk_fma_f32 v[68:69], v[88:89], s[10:11], v[68:69] op_sel:[1,1,0] op_sel_hi:[1,0,1] neg_lo:[0,1,0]
	v_pk_mul_f32 v[108:109], v[70:71], s[14:15] op_sel:[0,0] op_sel_hi:[0,1]
	v_pk_fma_f32 v[108:109], v[70:71], s[14:15], v[108:109] op_sel:[1,1,0] op_sel_hi:[1,0,1] neg_lo:[0,1,0]
	v_pk_add_f32 v[70:71], v[84:85], v[86:87] neg_lo:[0,1] neg_hi:[0,1]
	v_pk_mul_f32 v[106:107], v[64:65], s[12:13]
	v_pk_add_f32 v[64:65], v[84:85], v[86:87]
	v_pk_add_f32 v[74:75], v[76:77], v[90:91] neg_lo:[0,1] neg_hi:[0,1]
	v_pk_add_f32 v[88:89], v[64:65], v[72:73]
	v_pk_add_f32 v[72:73], v[64:65], v[72:73] neg_lo:[0,1] neg_hi:[0,1]
	v_pk_add_f32 v[80:81], v[70:71], v[74:75] op_sel:[0,1] op_sel_hi:[1,0] neg_hi:[0,1]
	v_pk_add_f32 v[64:65], v[70:71], v[74:75] op_sel:[0,1] op_sel_hi:[1,0] neg_lo:[0,1]
	v_pk_add_f32 v[70:71], v[100:101], v[66:67]
	v_pk_add_f32 v[66:67], v[100:101], v[66:67] neg_lo:[0,1] neg_hi:[0,1]
	v_pk_add_f32 v[74:75], v[82:83], v[68:69]
	v_pk_add_f32 v[68:69], v[82:83], v[68:69] neg_lo:[0,1] neg_hi:[0,1]
	v_pk_add_f32 v[90:91], v[70:71], v[74:75]
	v_pk_add_f32 v[74:75], v[70:71], v[74:75] neg_lo:[0,1] neg_hi:[0,1]
	v_pk_add_f32 v[82:83], v[66:67], v[68:69] op_sel:[0,1] op_sel_hi:[1,0] neg_hi:[0,1]
	v_pk_add_f32 v[66:67], v[66:67], v[68:69] op_sel:[0,1] op_sel_hi:[1,0] neg_lo:[0,1]
	v_pk_add_f32 v[68:69], v[98:99], v[78:79] op_sel:[0,1] op_sel_hi:[1,0] neg_hi:[0,1]
	v_pk_add_f32 v[70:71], v[98:99], v[78:79] op_sel:[0,1] op_sel_hi:[1,0] neg_lo:[0,1]
	v_pk_add_f32 v[76:77], v[92:93], v[106:107]
	v_pk_add_f32 v[78:79], v[92:93], v[106:107] neg_lo:[0,1] neg_hi:[0,1]
	v_pk_add_f32 v[92:93], v[76:77], v[68:69]
	v_pk_add_f32 v[76:77], v[68:69], v[76:77] neg_lo:[0,1] neg_hi:[0,1]
	v_pk_add_f32 v[86:87], v[70:71], v[78:79] op_sel:[0,1] op_sel_hi:[1,0] neg_hi:[0,1]
	v_pk_add_f32 v[68:69], v[70:71], v[78:79] op_sel:[0,1] op_sel_hi:[1,0] neg_lo:[0,1]
	v_pk_add_f32 v[70:71], v[102:103], v[104:105]
	v_pk_add_f32 v[98:99], v[102:103], v[104:105] neg_lo:[0,1] neg_hi:[0,1]
	v_pk_add_f32 v[78:79], v[94:95], v[108:109]
	v_pk_add_f32 v[100:101], v[94:95], v[108:109] neg_lo:[0,1] neg_hi:[0,1]
	v_pk_add_f32 v[94:95], v[70:71], v[78:79]
	v_pk_add_f32 v[78:79], v[70:71], v[78:79] neg_lo:[0,1] neg_hi:[0,1]
	v_pk_add_f32 v[84:85], v[98:99], v[100:101] op_sel:[0,1] op_sel_hi:[1,0] neg_hi:[0,1]
	v_pk_add_f32 v[70:71], v[98:99], v[100:101] op_sel:[0,1] op_sel_hi:[1,0] neg_lo:[0,1]
	v_mov_b32_e32 v98, v0
	s_nop 0
	v_and_b32_e32 v97, -16, v98
	v_and_b32_e32 v99, 15, v98
	v_lshlrev_b32_e32 v100, 3, v97
	v_mad_u32_u24 v100, v99, s5, v100
	v_cmp_ne_u32_e32 vcc, 0, v99
	ds_write2_b64 v100, v[88:89], v[90:91] offset1:1
	ds_write2_b64 v100, v[92:93], v[94:95] offset0:2 offset1:3
	ds_write2_b64 v100, v[80:81], v[82:83] offset0:4 offset1:5
	ds_write2_b64 v100, v[86:87], v[84:85] offset0:6 offset1:7
	ds_write2_b64 v100, v[72:73], v[74:75] offset0:8 offset1:9
	ds_write2_b64 v100, v[76:77], v[78:79] offset0:10 offset1:11
	ds_write2_b64 v100, v[64:65], v[66:67] offset0:12 offset1:13
	ds_write2_b64 v100, v[68:69], v[70:71] offset0:14 offset1:15
	s_waitcnt lgkmcnt(0)
	s_barrier
	s_and_saveexec_b64 s[6:7], vcc
	s_xor_b64 s[6:7], exec, s[6:7]
	v_sub_u32_e32 v99, 16, v99
	v_mul_u32_u24_e32 v99, 0x111, v99
	v_sub_u32_e32 v97, v99, v97
	v_add_u32_e32 v100, 0xf0, v97
	s_andn2_saveexec_b64 s[6:7], s[6:7]
	v_sub_u32_e32 v97, 0x100, v98
	v_cmp_lt_u32_e32 vcc, 15, v98
	s_nop 1
	v_cndmask_b32_e32 v100, 1, v97, vcc
	s_or_b64 exec, exec, s[6:7]
	v_mov_b32_e32 v97, 0
	v_lshlrev_b32_e32 v110, 3, v100
	ds_read_b64 v[108:109], v97
	ds_read2_b64 v[100:103], v110 offset0:14 offset1:15
	v_cmp_eq_u32_e32 vcc, 0, v98
	ds_read2_b64 v[104:107], v110 offset0:12 offset1:13
	s_mov_b32 s6, 0x3f6c835e
	s_mov_b32 s7, 0xbec3ef15
	s_waitcnt lgkmcnt(1)
	v_cndmask_b32_e32 v99, v103, v109, vcc
	v_cndmask_b32_e32 v98, v102, v108, vcc
	v_pk_add_f32 v[102:103], v[88:89], v[98:99] neg_hi:[0,1]
	v_pk_add_f32 v[88:89], v[88:89], v[98:99] neg_lo:[0,1]
	s_mov_b32 s9, s8
	v_pk_mul_f32 v[98:99], v[102:103], v[88:89] op_sel:[0,0] op_sel_hi:[0,1]
	v_pk_fma_f32 v[98:99], v[102:103], v[88:89], v[98:99] op_sel:[1,1,0] op_sel_hi:[1,0,1] neg_hi:[0,1,0]
	v_pk_add_f32 v[88:89], v[90:91], v[100:101] neg_hi:[0,1]
	v_pk_add_f32 v[90:91], v[90:91], v[100:101] neg_lo:[0,1]
	s_mov_b32 s14, s11
	v_pk_add_f32 v[62:63], v[62:63], v[98:99] op_sel:[1,0] op_sel_hi:[0,1] neg_lo:[0,1] neg_hi:[1,1]
	v_pk_mul_f32 v[98:99], v[88:89], v[90:91] op_sel:[0,0] op_sel_hi:[0,1]
	v_pk_fma_f32 v[98:99], v[88:89], v[90:91], v[98:99] op_sel:[1,1,0] op_sel_hi:[1,0,1] neg_hi:[0,1,0]
	s_waitcnt lgkmcnt(0)
	v_pk_add_f32 v[88:89], v[92:93], v[106:107] neg_hi:[0,1]
	v_pk_add_f32 v[90:91], v[92:93], v[106:107] neg_lo:[0,1]
	s_mov_b32 s15, s10
	v_pk_mul_f32 v[92:93], v[88:89], v[90:91] op_sel:[0,0] op_sel_hi:[0,1]
	v_pk_fma_f32 v[92:93], v[88:89], v[90:91], v[92:93] op_sel:[1,1,0] op_sel_hi:[1,0,1] neg_hi:[0,1,0]
	v_pk_add_f32 v[60:61], v[60:61], v[98:99] op_sel:[1,0] op_sel_hi:[0,1] neg_lo:[0,1] neg_hi:[1,1]
	ds_read2_b64 v[88:91], v110 offset0:10 offset1:11
	v_pk_add_f32 v[58:59], v[58:59], v[92:93] op_sel:[1,0] op_sel_hi:[0,1] neg_lo:[0,1] neg_hi:[1,1]
	v_pk_add_f32 v[92:93], v[94:95], v[104:105] neg_hi:[0,1]
	v_pk_add_f32 v[94:95], v[94:95], v[104:105] neg_lo:[0,1]
	s_mov_b32 s13, s12
	v_pk_mul_f32 v[98:99], v[92:93], v[94:95] op_sel:[0,0] op_sel_hi:[0,1]
	v_pk_fma_f32 v[98:99], v[92:93], v[94:95], v[98:99] op_sel:[1,1,0] op_sel_hi:[1,0,1] neg_hi:[0,1,0]
	ds_read2_b64 v[92:95], v110 offset0:8 offset1:9
	v_pk_add_f32 v[56:57], v[56:57], v[98:99] op_sel:[1,0] op_sel_hi:[0,1] neg_lo:[0,1] neg_hi:[1,1]
	s_waitcnt lgkmcnt(1)
	v_pk_add_f32 v[98:99], v[80:81], v[90:91] neg_hi:[0,1]
	v_pk_add_f32 v[80:81], v[80:81], v[90:91] neg_lo:[0,1]
	s_add_u32 s2, s2, 0x2000000
	v_pk_mul_f32 v[90:91], v[98:99], v[80:81] op_sel:[0,0] op_sel_hi:[0,1]
	v_pk_fma_f32 v[90:91], v[98:99], v[80:81], v[90:91] op_sel:[1,1,0] op_sel_hi:[1,0,1] neg_hi:[0,1,0]
	v_pk_add_f32 v[80:81], v[82:83], v[88:89] neg_hi:[0,1]
	v_pk_add_f32 v[82:83], v[82:83], v[88:89] neg_lo:[0,1]
	s_addc_u32 s3, s3, 0
	v_pk_mul_f32 v[88:89], v[80:81], v[82:83] op_sel:[0,0] op_sel_hi:[0,1]
	v_pk_fma_f32 v[88:89], v[80:81], v[82:83], v[88:89] op_sel:[1,1,0] op_sel_hi:[1,0,1] neg_hi:[0,1,0]
	s_waitcnt lgkmcnt(0)
	v_pk_add_f32 v[80:81], v[86:87], v[94:95] neg_lo:[0,1]
	v_pk_add_f32 v[54:55], v[54:55], v[90:91] op_sel:[1,0] op_sel_hi:[0,1] neg_lo:[0,1] neg_hi:[1,1]
	s_load_dwordx2 s[0:1], s[0:1], 0x8
	v_pk_add_f32 v[88:89], v[52:53], v[88:89] op_sel:[1,0] op_sel_hi:[0,1] neg_lo:[0,1] neg_hi:[1,1]
	v_pk_add_f32 v[52:53], v[86:87], v[94:95] neg_hi:[0,1]
	s_nop 0
	v_pk_mul_f32 v[82:83], v[52:53], v[80:81] op_sel:[0,0] op_sel_hi:[0,1]
	v_pk_fma_f32 v[82:83], v[52:53], v[80:81], v[82:83] op_sel:[1,1,0] op_sel_hi:[1,0,1] neg_hi:[0,1,0]
	v_pk_add_f32 v[80:81], v[84:85], v[92:93] neg_hi:[0,1]
	s_nop 0
	v_pk_add_f32 v[86:87], v[50:51], v[82:83] op_sel:[1,0] op_sel_hi:[0,1] neg_lo:[0,1] neg_hi:[1,1]
	ds_read2_b64 v[50:53], v110 offset0:6 offset1:7
	v_pk_add_f32 v[82:83], v[84:85], v[92:93] neg_lo:[0,1]
	s_nop 0
	v_pk_mul_f32 v[84:85], v[80:81], v[82:83] op_sel:[0,0] op_sel_hi:[0,1]
	v_pk_fma_f32 v[84:85], v[80:81], v[82:83], v[84:85] op_sel:[1,1,0] op_sel_hi:[1,0,1] neg_hi:[0,1,0]
	ds_read2_b64 v[80:83], v110 offset0:4 offset1:5
	v_pk_add_f32 v[84:85], v[48:49], v[84:85] op_sel:[1,0] op_sel_hi:[0,1] neg_lo:[0,1] neg_hi:[1,1]
	s_waitcnt lgkmcnt(0)
	v_pk_add_f32 v[48:49], v[72:73], v[52:53] neg_hi:[0,1]
	v_pk_add_f32 v[52:53], v[72:73], v[52:53] neg_lo:[0,1]
	s_nop 0
	v_pk_mul_f32 v[72:73], v[48:49], v[52:53] op_sel:[0,0] op_sel_hi:[0,1]
	v_pk_fma_f32 v[72:73], v[48:49], v[52:53], v[72:73] op_sel:[1,1,0] op_sel_hi:[1,0,1] neg_hi:[0,1,0]
	v_pk_add_f32 v[48:49], v[74:75], v[50:51] neg_lo:[0,1]
	s_nop 0
	v_pk_add_f32 v[52:53], v[46:47], v[72:73] op_sel:[1,0] op_sel_hi:[0,1] neg_lo:[0,1] neg_hi:[1,1]
	v_pk_add_f32 v[46:47], v[74:75], v[50:51] neg_hi:[0,1]
	s_nop 0
	v_pk_mul_f32 v[50:51], v[46:47], v[48:49] op_sel:[0,0] op_sel_hi:[0,1]
	v_pk_fma_f32 v[50:51], v[46:47], v[48:49], v[50:51] op_sel:[1,1,0] op_sel_hi:[1,0,1] neg_hi:[0,1,0]
	v_pk_add_f32 v[46:47], v[76:77], v[82:83] neg_lo:[0,1]
	s_nop 0
	v_pk_add_f32 v[50:51], v[44:45], v[50:51] op_sel:[1,0] op_sel_hi:[0,1] neg_lo:[0,1] neg_hi:[1,1]
	v_pk_add_f32 v[44:45], v[76:77], v[82:83] neg_hi:[0,1]
	s_nop 0
	v_pk_mul_f32 v[48:49], v[44:45], v[46:47] op_sel:[0,0] op_sel_hi:[0,1]
	v_pk_fma_f32 v[48:49], v[44:45], v[46:47], v[48:49] op_sel:[1,1,0] op_sel_hi:[1,0,1] neg_hi:[0,1,0]
	v_pk_add_f32 v[46:47], v[78:79], v[80:81] neg_hi:[0,1]
	s_nop 0
	v_pk_add_f32 v[72:73], v[42:43], v[48:49] op_sel:[1,0] op_sel_hi:[0,1] neg_lo:[0,1] neg_hi:[1,1]
	ds_read2_b64 v[42:45], v110 offset0:2 offset1:3
	v_pk_add_f32 v[48:49], v[78:79], v[80:81] neg_lo:[0,1]
	s_nop 0
	v_pk_mul_f32 v[74:75], v[46:47], v[48:49] op_sel:[0,0] op_sel_hi:[0,1]
	v_pk_fma_f32 v[74:75], v[46:47], v[48:49], v[74:75] op_sel:[1,1,0] op_sel_hi:[1,0,1] neg_hi:[0,1,0]
	ds_read2_b64 v[46:49], v110 offset1:1
	v_pk_add_f32 v[40:41], v[40:41], v[74:75] op_sel:[1,0] op_sel_hi:[0,1] neg_lo:[0,1] neg_hi:[1,1]
	s_waitcnt lgkmcnt(1)
	v_pk_add_f32 v[74:75], v[64:65], v[44:45] neg_hi:[0,1]
	v_pk_add_f32 v[44:45], v[64:65], v[44:45] neg_lo:[0,1]
	s_waitcnt lgkmcnt(0)
	v_pk_mul_f32 v[64:65], v[74:75], v[44:45] op_sel:[0,0] op_sel_hi:[0,1]
	v_pk_fma_f32 v[64:65], v[74:75], v[44:45], v[64:65] op_sel:[1,1,0] op_sel_hi:[1,0,1] neg_hi:[0,1,0]
	v_pk_add_f32 v[44:45], v[66:67], v[42:43] neg_hi:[0,1]
	v_pk_add_f32 v[42:43], v[66:67], v[42:43] neg_lo:[0,1]
	s_barrier
	v_pk_add_f32 v[38:39], v[38:39], v[64:65] op_sel:[1,0] op_sel_hi:[0,1] neg_lo:[0,1] neg_hi:[1,1]
	v_pk_mul_f32 v[64:65], v[44:45], v[42:43] op_sel:[0,0] op_sel_hi:[0,1]
	v_pk_fma_f32 v[64:65], v[44:45], v[42:43], v[64:65] op_sel:[1,1,0] op_sel_hi:[1,0,1] neg_hi:[0,1,0]
	v_pk_add_f32 v[42:43], v[68:69], v[48:49] neg_hi:[0,1]
	v_pk_add_f32 v[44:45], v[68:69], v[48:49] neg_lo:[0,1]
	s_nop 0
	v_pk_mul_f32 v[48:49], v[42:43], v[44:45] op_sel:[0,0] op_sel_hi:[0,1]
	v_pk_fma_f32 v[48:49], v[42:43], v[44:45], v[48:49] op_sel:[1,1,0] op_sel_hi:[1,0,1] neg_hi:[0,1,0]
	v_pk_add_f32 v[42:43], v[70:71], v[46:47] neg_hi:[0,1]
	v_pk_add_f32 v[44:45], v[70:71], v[46:47] neg_lo:[0,1]
	v_pk_add_f32 v[36:37], v[36:37], v[64:65] op_sel:[1,0] op_sel_hi:[0,1] neg_lo:[0,1] neg_hi:[1,1]
	s_nop 0
	v_pk_mul_f32 v[46:47], v[42:43], v[44:45] op_sel:[0,0] op_sel_hi:[0,1]
	v_pk_fma_f32 v[46:47], v[42:43], v[44:45], v[46:47] op_sel:[1,1,0] op_sel_hi:[1,0,1] neg_hi:[0,1,0]
	v_pk_add_f32 v[42:43], v[62:63], v[52:53]
	v_pk_add_f32 v[32:33], v[32:33], v[46:47] op_sel:[1,0] op_sel_hi:[0,1] neg_lo:[0,1] neg_hi:[1,1]
	v_pk_add_f32 v[44:45], v[62:63], v[52:53] neg_lo:[0,1] neg_hi:[0,1]
	v_pk_add_f32 v[46:47], v[54:55], v[38:39]
	v_pk_add_f32 v[38:39], v[54:55], v[38:39] neg_lo:[0,1] neg_hi:[0,1]
	v_pk_add_f32 v[34:35], v[34:35], v[48:49] op_sel:[1,0] op_sel_hi:[0,1] neg_lo:[0,1] neg_hi:[1,1]
	v_pk_add_f32 v[48:49], v[42:43], v[46:47]
	v_pk_add_f32 v[42:43], v[42:43], v[46:47] neg_lo:[0,1] neg_hi:[0,1]
	v_pk_add_f32 v[46:47], v[44:45], v[38:39] op_sel:[0,1] op_sel_hi:[1,0] neg_hi:[0,1]
	v_pk_add_f32 v[38:39], v[44:45], v[38:39] op_sel:[0,1] op_sel_hi:[1,0] neg_lo:[0,1]
	v_pk_add_f32 v[44:45], v[60:61], v[50:51]
	v_pk_add_f32 v[50:51], v[60:61], v[50:51] neg_lo:[0,1] neg_hi:[0,1]
	v_pk_add_f32 v[52:53], v[88:89], v[36:37]
	v_pk_add_f32 v[36:37], v[88:89], v[36:37] neg_lo:[0,1] neg_hi:[0,1]
	v_pk_add_f32 v[54:55], v[44:45], v[52:53]
	v_pk_add_f32 v[44:45], v[44:45], v[52:53] neg_lo:[0,1] neg_hi:[0,1]
	v_pk_add_f32 v[52:53], v[50:51], v[36:37] op_sel:[0,1] op_sel_hi:[1,0] neg_hi:[0,1]
	v_pk_add_f32 v[36:37], v[50:51], v[36:37] op_sel:[0,1] op_sel_hi:[1,0] neg_lo:[0,1]
	v_pk_add_f32 v[50:51], v[58:59], v[72:73]
	v_pk_add_f32 v[58:59], v[58:59], v[72:73] neg_lo:[0,1] neg_hi:[0,1]
	v_pk_add_f32 v[60:61], v[86:87], v[34:35]
	v_pk_add_f32 v[34:35], v[86:87], v[34:35] neg_lo:[0,1] neg_hi:[0,1]
	v_pk_add_f32 v[62:63], v[50:51], v[60:61]
	v_pk_add_f32 v[50:51], v[50:51], v[60:61] neg_lo:[0,1] neg_hi:[0,1]
	v_pk_add_f32 v[60:61], v[58:59], v[34:35] op_sel:[0,1] op_sel_hi:[1,0] neg_hi:[0,1]
	v_pk_add_f32 v[34:35], v[58:59], v[34:35] op_sel:[0,1] op_sel_hi:[1,0] neg_lo:[0,1]
	v_pk_add_f32 v[58:59], v[56:57], v[40:41]
	v_pk_add_f32 v[40:41], v[56:57], v[40:41] neg_lo:[0,1] neg_hi:[0,1]
	v_pk_add_f32 v[56:57], v[84:85], v[32:33]
	v_pk_add_f32 v[32:33], v[84:85], v[32:33] neg_lo:[0,1] neg_hi:[0,1]
	v_pk_add_f32 v[64:65], v[58:59], v[56:57]
	v_pk_add_f32 v[56:57], v[58:59], v[56:57] neg_lo:[0,1] neg_hi:[0,1]
	v_pk_add_f32 v[58:59], v[40:41], v[32:33] op_sel:[0,1] op_sel_hi:[1,0] neg_hi:[0,1]
	v_pk_add_f32 v[32:33], v[40:41], v[32:33] op_sel:[0,1] op_sel_hi:[1,0] neg_lo:[0,1]
	v_pk_mul_f32 v[40:41], v[52:53], s[6:7] op_sel:[0,0] op_sel_hi:[0,1]
	v_pk_fma_f32 v[40:41], v[52:53], s[6:7], v[40:41] op_sel:[1,1,0] op_sel_hi:[1,0,1] neg_lo:[0,1,0]
	v_pk_mul_f32 v[52:53], v[36:37], s[10:11] op_sel:[0,0] op_sel_hi:[0,1]
	v_pk_fma_f32 v[52:53], v[36:37], s[10:11], v[52:53] op_sel:[1,1,0] op_sel_hi:[1,0,1] neg_lo:[0,1,0]
	v_pk_add_f32 v[36:37], v[60:61], v[60:61] op_sel:[0,1] op_sel_hi:[1,0] neg_hi:[0,1]
	v_pk_add_f32 v[44:45], v[44:45], v[44:45] op_sel:[0,1] op_sel_hi:[1,0] neg_hi:[0,1]
	s_nop 0
	v_pk_mul_f32 v[60:61], v[58:59], s[10:11] op_sel:[0,0] op_sel_hi:[0,1]
	v_pk_fma_f32 v[60:61], v[58:59], s[10:11], v[60:61] op_sel:[1,1,0] op_sel_hi:[1,0,1] neg_lo:[0,1,0]
	v_pk_mul_f32 v[58:59], v[32:33], s[14:15] op_sel:[0,0] op_sel_hi:[0,1]
	v_pk_fma_f32 v[58:59], v[32:33], s[14:15], v[58:59] op_sel:[1,1,0] op_sel_hi:[1,0,1] neg_lo:[0,1,0]
	v_pk_add_f32 v[32:33], v[48:49], v[62:63]
	v_pk_mul_f32 v[36:37], v[36:37], s[8:9]
	v_pk_add_f32 v[48:49], v[48:49], v[62:63] neg_lo:[0,1] neg_hi:[0,1]
	v_pk_add_f32 v[62:63], v[54:55], v[64:65]
	v_pk_add_f32 v[54:55], v[54:55], v[64:65] neg_lo:[0,1] neg_hi:[0,1]
	v_pk_mul_f32 v[44:45], v[44:45], s[8:9]
	v_pk_add_f32 v[34:35], v[34:35], v[34:35] op_sel:[0,1] op_sel_hi:[1,0] neg_lo:[0,1]
	v_pk_add_f32 v[56:57], v[56:57], v[56:57] op_sel:[0,1] op_sel_hi:[1,0] neg_lo:[0,1]
	v_pk_add_f32 v[64:65], v[32:33], v[62:63]
	v_pk_add_f32 v[32:33], v[32:33], v[62:63] neg_lo:[0,1] neg_hi:[0,1]
	v_pk_add_f32 v[62:63], v[48:49], v[54:55] op_sel:[0,1] op_sel_hi:[1,0] neg_hi:[0,1]
	v_pk_add_f32 v[48:49], v[48:49], v[54:55] op_sel:[0,1] op_sel_hi:[1,0] neg_lo:[0,1]
	v_pk_add_f32 v[54:55], v[46:47], v[36:37]
	v_pk_add_f32 v[36:37], v[46:47], v[36:37] neg_lo:[0,1] neg_hi:[0,1]
	v_pk_add_f32 v[46:47], v[40:41], v[60:61]
	v_pk_add_f32 v[40:41], v[40:41], v[60:61] neg_lo:[0,1] neg_hi:[0,1]
	v_pk_mul_f32 v[34:35], v[34:35], s[12:13]
	v_pk_mul_f32 v[56:57], v[56:57], s[12:13]
	v_pk_add_f32 v[60:61], v[54:55], v[46:47]
	v_pk_add_f32 v[46:47], v[54:55], v[46:47] neg_lo:[0,1] neg_hi:[0,1]
	v_pk_add_f32 v[54:55], v[36:37], v[40:41] op_sel:[0,1] op_sel_hi:[1,0] neg_hi:[0,1]
	v_pk_add_f32 v[36:37], v[36:37], v[40:41] op_sel:[0,1] op_sel_hi:[1,0] neg_lo:[0,1]
	v_pk_add_f32 v[40:41], v[42:43], v[50:51] op_sel:[0,1] op_sel_hi:[1,0] neg_hi:[0,1]
	v_pk_add_f32 v[42:43], v[42:43], v[50:51] op_sel:[0,1] op_sel_hi:[1,0] neg_lo:[0,1]
	v_pk_add_f32 v[50:51], v[44:45], v[56:57]
	v_pk_add_f32 v[44:45], v[44:45], v[56:57] neg_lo:[0,1] neg_hi:[0,1]
	v_pk_add_f32 v[56:57], v[50:51], v[40:41]
	v_pk_add_f32 v[40:41], v[40:41], v[50:51] neg_lo:[0,1] neg_hi:[0,1]
	v_pk_add_f32 v[50:51], v[42:43], v[44:45] op_sel:[0,1] op_sel_hi:[1,0] neg_hi:[0,1]
	v_pk_add_f32 v[42:43], v[42:43], v[44:45] op_sel:[0,1] op_sel_hi:[1,0] neg_lo:[0,1]
	v_pk_add_f32 v[44:45], v[38:39], v[34:35]
	v_pk_add_f32 v[34:35], v[38:39], v[34:35] neg_lo:[0,1] neg_hi:[0,1]
	v_pk_add_f32 v[38:39], v[52:53], v[58:59]
	v_pk_add_f32 v[52:53], v[52:53], v[58:59] neg_lo:[0,1] neg_hi:[0,1]
	v_pk_add_f32 v[58:59], v[44:45], v[38:39]
	v_pk_add_f32 v[38:39], v[44:45], v[38:39] neg_lo:[0,1] neg_hi:[0,1]
	v_pk_add_f32 v[44:45], v[34:35], v[52:53] op_sel:[0,1] op_sel_hi:[1,0] neg_hi:[0,1]
	v_pk_add_f32 v[34:35], v[34:35], v[52:53] op_sel:[0,1] op_sel_hi:[1,0] neg_lo:[0,1]
	v_pk_mul_f32 v[52:53], v[60:61], v[30:31] op_sel:[0,0] op_sel_hi:[0,1]
	v_pk_fma_f32 v[52:53], v[60:61], v[30:31], v[52:53] op_sel:[1,1,0] op_sel_hi:[1,0,1] neg_lo:[0,1,0]
	v_pk_mul_f32 v[30:31], v[56:57], v[28:29] op_sel:[0,0] op_sel_hi:[0,1]
	v_pk_fma_f32 v[30:31], v[56:57], v[28:29], v[30:31] op_sel:[1,1,0] op_sel_hi:[1,0,1] neg_lo:[0,1,0]
	v_pk_mul_f32 v[28:29], v[58:59], v[26:27] op_sel:[0,0] op_sel_hi:[0,1]
	v_pk_fma_f32 v[28:29], v[58:59], v[26:27], v[28:29] op_sel:[1,1,0] op_sel_hi:[1,0,1] neg_lo:[0,1,0]
	v_pk_mul_f32 v[26:27], v[62:63], v[24:25] op_sel:[0,0] op_sel_hi:[0,1]
	v_pk_fma_f32 v[26:27], v[62:63], v[24:25], v[26:27] op_sel:[1,1,0] op_sel_hi:[1,0,1] neg_lo:[0,1,0]
	v_pk_mul_f32 v[24:25], v[54:55], v[20:21] op_sel:[0,0] op_sel_hi:[0,1]
	v_pk_fma_f32 v[24:25], v[54:55], v[20:21], v[24:25] op_sel:[1,1,0] op_sel_hi:[1,0,1] neg_lo:[0,1,0]
	v_pk_mul_f32 v[20:21], v[50:51], v[16:17] op_sel:[0,0] op_sel_hi:[0,1]
	v_pk_fma_f32 v[20:21], v[50:51], v[16:17], v[20:21] op_sel:[1,1,0] op_sel_hi:[1,0,1] neg_lo:[0,1,0]
	s_nop 0
	v_pk_mul_f32 v[16:17], v[44:45], v[10:11] op_sel:[0,0] op_sel_hi:[0,1]
	v_pk_fma_f32 v[16:17], v[44:45], v[10:11], v[16:17] op_sel:[1,1,0] op_sel_hi:[1,0,1] neg_lo:[0,1,0]
	v_pk_mul_f32 v[10:11], v[32:33], v[22:23] op_sel:[0,0] op_sel_hi:[0,1]
	v_pk_fma_f32 v[10:11], v[32:33], v[22:23], v[10:11] op_sel:[1,1,0] op_sel_hi:[1,0,1] neg_lo:[0,1,0]
	ds_write_b64 v1, v[10:11] offset:17472
	v_pk_mul_f32 v[10:11], v[46:47], v[18:19] op_sel:[0,0] op_sel_hi:[0,1]
	v_pk_fma_f32 v[10:11], v[46:47], v[18:19], v[10:11] op_sel:[1,1,0] op_sel_hi:[1,0,1] neg_lo:[0,1,0]
	ds_write_b64 v1, v[10:11] offset:19656
	v_pk_mul_f32 v[10:11], v[40:41], v[12:13] op_sel:[0,0] op_sel_hi:[0,1]
	v_pk_fma_f32 v[10:11], v[40:41], v[12:13], v[10:11] op_sel:[1,1,0] op_sel_hi:[1,0,1] neg_lo:[0,1,0]
	ds_write_b64 v1, v[10:11] offset:21840
	v_pk_mul_f32 v[10:11], v[38:39], v[14:15] op_sel:[0,0] op_sel_hi:[0,1]
	v_pk_fma_f32 v[10:11], v[38:39], v[14:15], v[10:11] op_sel:[1,1,0] op_sel_hi:[1,0,1] neg_lo:[0,1,0]
	ds_write_b64 v1, v[10:11] offset:24024
	v_pk_mul_f32 v[10:11], v[48:49], v[6:7] op_sel:[0,0] op_sel_hi:[0,1]
	v_pk_fma_f32 v[10:11], v[48:49], v[6:7], v[10:11] op_sel:[1,1,0] op_sel_hi:[1,0,1] neg_lo:[0,1,0]
	v_pk_mul_f32 v[6:7], v[36:37], v[8:9] op_sel:[0,0] op_sel_hi:[0,1]
	v_pk_fma_f32 v[6:7], v[36:37], v[8:9], v[6:7] op_sel:[1,1,0] op_sel_hi:[1,0,1] neg_lo:[0,1,0]
	ds_write_b64 v1, v[6:7] offset:28392
	v_pk_mul_f32 v[6:7], v[42:43], v[4:5] op_sel:[0,0] op_sel_hi:[0,1]
	v_pk_fma_f32 v[6:7], v[42:43], v[4:5], v[6:7] op_sel:[1,1,0] op_sel_hi:[1,0,1] neg_lo:[0,1,0]
	v_pk_mul_f32 v[4:5], v[34:35], v[2:3] op_sel:[0,0] op_sel_hi:[0,1]
	v_pk_fma_f32 v[4:5], v[34:35], v[2:3], v[4:5] op_sel:[1,1,0] op_sel_hi:[1,0,1] neg_lo:[0,1,0]
	ds_write_b64 v1, v[64:65]
	ds_write_b64 v1, v[52:53] offset:2184
	ds_write_b64 v1, v[30:31] offset:4368
	ds_write_b64 v1, v[28:29] offset:6552
	ds_write_b64 v1, v[26:27] offset:8736
	ds_write_b64 v1, v[24:25] offset:10920
	ds_write_b64 v1, v[20:21] offset:13104
	ds_write_b64 v1, v[16:17] offset:15288
	ds_write_b64 v1, v[10:11] offset:26208
	ds_write_b64 v1, v[6:7] offset:30576
	ds_write_b64 v1, v[4:5] offset:32760
	s_waitcnt lgkmcnt(0)
	s_barrier
	ds_read2_b64 v[2:5], v96 offset1:16
	ds_read2_b64 v[6:9], v96 offset0:32 offset1:48
	ds_read2_b64 v[10:13], v96 offset0:64 offset1:80
	ds_read2_b64 v[14:17], v96 offset0:128 offset1:144
	ds_read2_b64 v[18:21], v96 offset0:96 offset1:112
	ds_read2_b64 v[22:25], v96 offset0:192 offset1:208
	ds_read2_b64 v[26:29], v96 offset0:160 offset1:176
	ds_read2_b64 v[30:33], v96 offset0:224 offset1:240
	s_waitcnt lgkmcnt(4)
	v_pk_add_f32 v[34:35], v[2:3], v[14:15]
	v_pk_add_f32 v[2:3], v[2:3], v[14:15] neg_lo:[0,1] neg_hi:[0,1]
	s_waitcnt lgkmcnt(2)
	v_pk_add_f32 v[14:15], v[10:11], v[22:23]
	v_pk_add_f32 v[10:11], v[10:11], v[22:23] neg_lo:[0,1] neg_hi:[0,1]
	v_pk_add_f32 v[22:23], v[34:35], v[14:15]
	v_pk_add_f32 v[14:15], v[34:35], v[14:15] neg_lo:[0,1] neg_hi:[0,1]
	v_pk_add_f32 v[34:35], v[2:3], v[10:11] op_sel:[0,1] op_sel_hi:[1,0] neg_hi:[0,1]
	v_pk_add_f32 v[2:3], v[2:3], v[10:11] op_sel:[0,1] op_sel_hi:[1,0] neg_lo:[0,1]
	v_pk_add_f32 v[10:11], v[4:5], v[16:17]
	v_pk_add_f32 v[4:5], v[4:5], v[16:17] neg_lo:[0,1] neg_hi:[0,1]
	v_pk_add_f32 v[16:17], v[12:13], v[24:25]
	v_pk_add_f32 v[12:13], v[12:13], v[24:25] neg_lo:[0,1] neg_hi:[0,1]
	v_pk_add_f32 v[24:25], v[10:11], v[16:17]
	v_pk_add_f32 v[10:11], v[10:11], v[16:17] neg_lo:[0,1] neg_hi:[0,1]
	v_pk_add_f32 v[16:17], v[4:5], v[12:13] op_sel:[0,1] op_sel_hi:[1,0] neg_hi:[0,1]
	v_pk_add_f32 v[4:5], v[4:5], v[12:13] op_sel:[0,1] op_sel_hi:[1,0] neg_lo:[0,1]
	s_waitcnt lgkmcnt(1)
	v_pk_add_f32 v[12:13], v[6:7], v[26:27]
	v_pk_add_f32 v[6:7], v[6:7], v[26:27] neg_lo:[0,1] neg_hi:[0,1]
	s_waitcnt lgkmcnt(0)
	v_pk_add_f32 v[26:27], v[18:19], v[30:31]
	v_pk_add_f32 v[18:19], v[18:19], v[30:31] neg_lo:[0,1] neg_hi:[0,1]
	v_pk_add_f32 v[30:31], v[12:13], v[26:27]
	v_pk_add_f32 v[12:13], v[12:13], v[26:27] neg_lo:[0,1] neg_hi:[0,1]
	v_pk_add_f32 v[26:27], v[6:7], v[18:19] op_sel:[0,1] op_sel_hi:[1,0] neg_hi:[0,1]
	v_pk_add_f32 v[6:7], v[6:7], v[18:19] op_sel:[0,1] op_sel_hi:[1,0] neg_lo:[0,1]
	v_pk_add_f32 v[18:19], v[8:9], v[28:29]
	v_pk_add_f32 v[8:9], v[8:9], v[28:29] neg_lo:[0,1] neg_hi:[0,1]
	v_pk_add_f32 v[28:29], v[20:21], v[32:33]
	v_pk_add_f32 v[20:21], v[20:21], v[32:33] neg_lo:[0,1] neg_hi:[0,1]
	v_pk_add_f32 v[32:33], v[18:19], v[28:29]
	v_pk_add_f32 v[18:19], v[18:19], v[28:29] neg_lo:[0,1] neg_hi:[0,1]
	v_pk_add_f32 v[28:29], v[8:9], v[20:21] op_sel:[0,1] op_sel_hi:[1,0] neg_hi:[0,1]
	v_pk_add_f32 v[8:9], v[8:9], v[20:21] op_sel:[0,1] op_sel_hi:[1,0] neg_lo:[0,1]
	v_pk_mul_f32 v[20:21], v[16:17], s[6:7] op_sel:[0,0] op_sel_hi:[0,1]
	v_pk_fma_f32 v[20:21], v[16:17], s[6:7], v[20:21] op_sel:[1,1,0] op_sel_hi:[1,0,1] neg_lo:[0,1,0]
	v_pk_mul_f32 v[16:17], v[4:5], s[10:11] op_sel:[0,0] op_sel_hi:[0,1]
	v_pk_fma_f32 v[16:17], v[4:5], s[10:11], v[16:17] op_sel:[1,1,0] op_sel_hi:[1,0,1] neg_lo:[0,1,0]
	v_pk_add_f32 v[4:5], v[26:27], v[26:27] op_sel:[0,1] op_sel_hi:[1,0] neg_hi:[0,1]
	v_pk_add_f32 v[10:11], v[10:11], v[10:11] op_sel:[0,1] op_sel_hi:[1,0] neg_hi:[0,1]
	s_nop 0
	v_pk_mul_f32 v[26:27], v[28:29], s[10:11] op_sel:[0,0] op_sel_hi:[0,1]
	v_pk_fma_f32 v[26:27], v[28:29], s[10:11], v[26:27] op_sel:[1,1,0] op_sel_hi:[1,0,1] neg_lo:[0,1,0]
	v_pk_mul_f32 v[28:29], v[8:9], s[14:15] op_sel:[0,0] op_sel_hi:[0,1]
	v_pk_fma_f32 v[28:29], v[8:9], s[14:15], v[28:29] op_sel:[1,1,0] op_sel_hi:[1,0,1] neg_lo:[0,1,0]
	v_pk_add_f32 v[8:9], v[22:23], v[30:31]
	v_pk_mul_f32 v[4:5], v[4:5], s[8:9]
	v_pk_add_f32 v[22:23], v[22:23], v[30:31] neg_lo:[0,1] neg_hi:[0,1]
	v_pk_add_f32 v[30:31], v[24:25], v[32:33]
	v_pk_add_f32 v[24:25], v[24:25], v[32:33] neg_lo:[0,1] neg_hi:[0,1]
	v_pk_add_f32 v[18:19], v[18:19], v[18:19] op_sel:[0,1] op_sel_hi:[1,0] neg_lo:[0,1]
	v_pk_add_f32 v[32:33], v[8:9], v[30:31]
	v_pk_add_f32 v[30:31], v[8:9], v[30:31] neg_lo:[0,1] neg_hi:[0,1]
	v_pk_add_f32 v[36:37], v[22:23], v[24:25] op_sel:[0,1] op_sel_hi:[1,0] neg_hi:[0,1]
	v_pk_add_f32 v[22:23], v[22:23], v[24:25] op_sel:[0,1] op_sel_hi:[1,0] neg_lo:[0,1]
	v_pk_add_f32 v[8:9], v[34:35], v[4:5]
	v_pk_add_f32 v[4:5], v[34:35], v[4:5] neg_lo:[0,1] neg_hi:[0,1]
	v_pk_add_f32 v[24:25], v[20:21], v[26:27]
	v_pk_add_f32 v[20:21], v[20:21], v[26:27] neg_lo:[0,1] neg_hi:[0,1]
	v_pk_mul_f32 v[10:11], v[10:11], s[8:9]
	v_pk_add_f32 v[6:7], v[6:7], v[6:7] op_sel:[0,1] op_sel_hi:[1,0] neg_lo:[0,1]
	v_pk_mul_f32 v[18:19], v[18:19], s[12:13]
	v_pk_add_f32 v[26:27], v[8:9], v[24:25]
	v_pk_add_f32 v[24:25], v[8:9], v[24:25] neg_lo:[0,1] neg_hi:[0,1]
	v_pk_add_f32 v[34:35], v[4:5], v[20:21] op_sel:[0,1] op_sel_hi:[1,0] neg_hi:[0,1]
	v_pk_add_f32 v[20:21], v[4:5], v[20:21] op_sel:[0,1] op_sel_hi:[1,0] neg_lo:[0,1]
	v_pk_add_f32 v[4:5], v[14:15], v[12:13] op_sel:[0,1] op_sel_hi:[1,0] neg_hi:[0,1]
	v_pk_add_f32 v[8:9], v[14:15], v[12:13] op_sel:[0,1] op_sel_hi:[1,0] neg_lo:[0,1]
	v_pk_add_f32 v[12:13], v[10:11], v[18:19]
	v_pk_mul_f32 v[6:7], v[6:7], s[12:13]
	v_pk_add_f32 v[10:11], v[10:11], v[18:19] neg_lo:[0,1] neg_hi:[0,1]
	v_pk_add_f32 v[14:15], v[12:13], v[4:5]
	v_pk_add_f32 v[12:13], v[4:5], v[12:13] neg_lo:[0,1] neg_hi:[0,1]
	v_pk_add_f32 v[4:5], v[2:3], v[6:7]
	v_pk_add_f32 v[2:3], v[2:3], v[6:7] neg_lo:[0,1] neg_hi:[0,1]
	v_mov_b32_e32 v1, v0
	v_pk_add_f32 v[18:19], v[8:9], v[10:11] op_sel:[0,1] op_sel_hi:[1,0] neg_hi:[0,1]
	v_pk_add_f32 v[10:11], v[8:9], v[10:11] op_sel:[0,1] op_sel_hi:[1,0] neg_lo:[0,1]
	v_pk_add_f32 v[8:9], v[16:17], v[28:29] neg_lo:[0,1] neg_hi:[0,1]
	v_pk_add_f32 v[6:7], v[16:17], v[28:29]
	v_pk_add_f32 v[38:39], v[2:3], v[8:9] op_sel:[0,1] op_sel_hi:[1,0] neg_hi:[0,1]
	v_pk_add_f32 v[40:41], v[2:3], v[8:9] op_sel:[0,1] op_sel_hi:[1,0] neg_lo:[0,1]
	v_ashrrev_i32_e32 v2, 4, v1
	v_lshlrev_b32_e32 v44, 3, v2
	v_add_u32_e32 v45, 0x8800, v44
	v_and_b32_e32 v1, 15, v1
	v_pk_add_f32 v[16:17], v[4:5], v[6:7]
	v_pk_add_f32 v[28:29], v[4:5], v[6:7] neg_lo:[0,1] neg_hi:[0,1]
	ds_read2_b64 v[2:5], v45 offset0:16 offset1:32
	v_mad_u32_u24 v1, v1, s5, v44
	ds_read2_b64 v[6:9], v45 offset0:48 offset1:64
	s_waitcnt lgkmcnt(1)
	v_pk_mul_f32 v[42:43], v[26:27], v[2:3] op_sel:[0,0] op_sel_hi:[0,1]
	v_pk_fma_f32 v[42:43], v[26:27], v[2:3], v[42:43] op_sel:[1,1,0] op_sel_hi:[1,0,1] neg_lo:[0,1,0]
	v_pk_mul_f32 v[26:27], v[14:15], v[4:5] op_sel:[0,0] op_sel_hi:[0,1]
	v_pk_fma_f32 v[26:27], v[14:15], v[4:5], v[26:27] op_sel:[1,1,0] op_sel_hi:[1,0,1] neg_lo:[0,1,0]
	s_waitcnt lgkmcnt(0)
	v_pk_mul_f32 v[14:15], v[16:17], v[6:7] op_sel:[0,0] op_sel_hi:[0,1]
	v_pk_fma_f32 v[14:15], v[16:17], v[6:7], v[14:15] op_sel:[1,1,0] op_sel_hi:[1,0,1] neg_lo:[0,1,0]
	ds_write2_b64 v1, v[26:27], v[14:15] offset0:32 offset1:48
	v_pk_mul_f32 v[14:15], v[36:37], v[8:9] op_sel:[0,0] op_sel_hi:[0,1]
	v_pk_fma_f32 v[14:15], v[36:37], v[8:9], v[14:15] op_sel:[1,1,0] op_sel_hi:[1,0,1] neg_lo:[0,1,0]
	ds_read2_b64 v[2:5], v45 offset0:80 offset1:96
	s_waitcnt lgkmcnt(0)
	v_pk_mul_f32 v[16:17], v[34:35], v[2:3] op_sel:[0,0] op_sel_hi:[0,1]
	v_pk_fma_f32 v[16:17], v[34:35], v[2:3], v[16:17] op_sel:[1,1,0] op_sel_hi:[1,0,1] neg_lo:[0,1,0]
	ds_write2_b64 v1, v[14:15], v[16:17] offset0:64 offset1:80
	v_pk_mul_f32 v[14:15], v[18:19], v[4:5] op_sel:[0,0] op_sel_hi:[0,1]
	v_pk_fma_f32 v[14:15], v[18:19], v[4:5], v[14:15] op_sel:[1,1,0] op_sel_hi:[1,0,1] neg_lo:[0,1,0]
	ds_read2_b64 v[6:9], v45 offset0:112 offset1:128
	ds_read2_b64 v[2:5], v45 offset0:144 offset1:160
	s_waitcnt lgkmcnt(1)
	v_pk_mul_f32 v[16:17], v[38:39], v[6:7] op_sel:[0,0] op_sel_hi:[0,1]
	v_pk_fma_f32 v[16:17], v[38:39], v[6:7], v[16:17] op_sel:[1,1,0] op_sel_hi:[1,0,1] neg_lo:[0,1,0]
	ds_write2_b64 v1, v[14:15], v[16:17] offset0:96 offset1:112
	v_pk_mul_f32 v[14:15], v[30:31], v[8:9] op_sel:[0,0] op_sel_hi:[0,1]
	v_pk_fma_f32 v[14:15], v[30:31], v[8:9], v[14:15] op_sel:[1,1,0] op_sel_hi:[1,0,1] neg_lo:[0,1,0]
	ds_read2_b64 v[6:9], v45 offset0:176 offset1:192
	s_waitcnt lgkmcnt(2)
	v_pk_mul_f32 v[16:17], v[24:25], v[2:3] op_sel:[0,0] op_sel_hi:[0,1]
	v_pk_fma_f32 v[16:17], v[24:25], v[2:3], v[16:17] op_sel:[1,1,0] op_sel_hi:[1,0,1] neg_lo:[0,1,0]
	ds_write2_b64 v1, v[14:15], v[16:17] offset0:128 offset1:144
	v_pk_mul_f32 v[14:15], v[12:13], v[4:5] op_sel:[0,0] op_sel_hi:[0,1]
	v_pk_fma_f32 v[14:15], v[12:13], v[4:5], v[14:15] op_sel:[1,1,0] op_sel_hi:[1,0,1] neg_lo:[0,1,0]
	ds_read2_b64 v[2:5], v45 offset0:208 offset1:224
	s_waitcnt lgkmcnt(2)
	v_pk_mul_f32 v[12:13], v[28:29], v[6:7] op_sel:[0,0] op_sel_hi:[0,1]
	v_pk_fma_f32 v[12:13], v[28:29], v[6:7], v[12:13] op_sel:[1,1,0] op_sel_hi:[1,0,1] neg_lo:[0,1,0]
	ds_write2_b64 v1, v[32:33], v[42:43] offset1:16
	ds_write2_b64 v1, v[14:15], v[12:13] offset0:160 offset1:176
	ds_read_b64 v[6:7], v44 offset:36736
	v_pk_mul_f32 v[12:13], v[22:23], v[8:9] op_sel:[0,0] op_sel_hi:[0,1]
	v_pk_fma_f32 v[12:13], v[22:23], v[8:9], v[12:13] op_sel:[1,1,0] op_sel_hi:[1,0,1] neg_lo:[0,1,0]
	s_waitcnt lgkmcnt(3)
	v_pk_mul_f32 v[8:9], v[20:21], v[2:3] op_sel:[0,0] op_sel_hi:[0,1]
	v_pk_fma_f32 v[8:9], v[20:21], v[2:3], v[8:9] op_sel:[1,1,0] op_sel_hi:[1,0,1] neg_lo:[0,1,0]
	ds_write2_b64 v1, v[12:13], v[8:9] offset0:192 offset1:208
	v_pk_mul_f32 v[2:3], v[10:11], v[4:5] op_sel:[0,0] op_sel_hi:[0,1]
	v_pk_fma_f32 v[2:3], v[10:11], v[4:5], v[2:3] op_sel:[1,1,0] op_sel_hi:[1,0,1] neg_lo:[0,1,0]
	s_waitcnt lgkmcnt(1)
	v_pk_mul_f32 v[4:5], v[40:41], v[6:7] op_sel:[0,0] op_sel_hi:[0,1]
	v_pk_fma_f32 v[4:5], v[40:41], v[6:7], v[4:5] op_sel:[1,1,0] op_sel_hi:[1,0,1] neg_lo:[0,1,0]
	ds_write2_b64 v1, v[2:3], v[4:5] offset0:224 offset1:240
	v_mov_b32_e32 v1, v0
	s_waitcnt lgkmcnt(0)
	s_barrier
	v_mov_b32_e32 v53, 0
	v_and_b32_e32 v2, 15, v1
	v_and_b32_e32 v1, 0x1ffffff0, v1
	v_lshlrev_b32_e32 v1, 3, v1
	v_mad_u32_u24 v1, v2, s5, v1
	ds_read2_b64 v[2:5], v1 offset1:1
	ds_read2_b64 v[6:9], v1 offset0:2 offset1:3
	ds_read2_b64 v[10:13], v1 offset0:8 offset1:9
	ds_read2_b64 v[18:21], v1 offset0:4 offset1:5
	ds_read2_b64 v[22:25], v1 offset0:6 offset1:7
	ds_read2_b64 v[26:29], v1 offset0:12 offset1:13
	ds_read2_b64 v[30:33], v1 offset0:10 offset1:11
	ds_read2_b64 v[34:37], v1 offset0:14 offset1:15
	s_waitcnt lgkmcnt(5)
	v_pk_add_f32 v[14:15], v[2:3], v[10:11]
	v_pk_add_f32 v[2:3], v[2:3], v[10:11] neg_lo:[0,1] neg_hi:[0,1]
	s_waitcnt lgkmcnt(2)
	v_pk_add_f32 v[10:11], v[18:19], v[26:27]
	v_pk_add_f32 v[18:19], v[18:19], v[26:27] neg_lo:[0,1] neg_hi:[0,1]
	v_pk_add_f32 v[26:27], v[14:15], v[10:11]
	v_pk_add_f32 v[16:17], v[14:15], v[10:11] neg_lo:[0,1] neg_hi:[0,1]
	v_pk_add_f32 v[14:15], v[2:3], v[18:19] op_sel:[0,1] op_sel_hi:[1,0] neg_hi:[0,1]
	v_pk_add_f32 v[18:19], v[2:3], v[18:19] op_sel:[0,1] op_sel_hi:[1,0] neg_lo:[0,1]
	v_pk_add_f32 v[2:3], v[4:5], v[12:13]
	v_pk_add_f32 v[10:11], v[20:21], v[28:29]
	v_pk_add_f32 v[4:5], v[4:5], v[12:13] neg_lo:[0,1] neg_hi:[0,1]
	v_pk_add_f32 v[12:13], v[20:21], v[28:29] neg_lo:[0,1] neg_hi:[0,1]
	v_pk_add_f32 v[28:29], v[2:3], v[10:11]
	v_pk_add_f32 v[2:3], v[2:3], v[10:11] neg_lo:[0,1] neg_hi:[0,1]
	v_pk_add_f32 v[10:11], v[4:5], v[12:13] op_sel:[0,1] op_sel_hi:[1,0] neg_hi:[0,1]
	v_pk_add_f32 v[4:5], v[4:5], v[12:13] op_sel:[0,1] op_sel_hi:[1,0] neg_lo:[0,1]
	s_waitcnt lgkmcnt(1)
	v_pk_add_f32 v[12:13], v[6:7], v[30:31]
	s_waitcnt lgkmcnt(0)
	v_pk_add_f32 v[20:21], v[22:23], v[34:35]
	v_pk_add_f32 v[2:3], v[2:3], v[2:3] op_sel:[0,1] op_sel_hi:[1,0] neg_hi:[0,1]
	v_pk_add_f32 v[6:7], v[6:7], v[30:31] neg_lo:[0,1] neg_hi:[0,1]
	v_pk_add_f32 v[22:23], v[22:23], v[34:35] neg_lo:[0,1] neg_hi:[0,1]
	v_pk_add_f32 v[30:31], v[12:13], v[20:21]
	v_pk_add_f32 v[20:21], v[12:13], v[20:21] neg_lo:[0,1] neg_hi:[0,1]
	v_pk_add_f32 v[12:13], v[6:7], v[22:23] op_sel:[0,1] op_sel_hi:[1,0] neg_hi:[0,1]
	v_pk_mul_f32 v[44:45], v[2:3], s[8:9]
	v_pk_add_f32 v[6:7], v[6:7], v[22:23] op_sel:[0,1] op_sel_hi:[1,0] neg_lo:[0,1]
	v_pk_add_f32 v[22:23], v[8:9], v[32:33]
	v_pk_add_f32 v[2:3], v[12:13], v[12:13] op_sel:[0,1] op_sel_hi:[1,0] neg_hi:[0,1]
	v_pk_add_f32 v[8:9], v[8:9], v[32:33] neg_lo:[0,1] neg_hi:[0,1]
	v_pk_add_f32 v[32:33], v[24:25], v[36:37]
	v_pk_mul_f32 v[12:13], v[2:3], s[8:9]
	v_pk_add_f32 v[2:3], v[6:7], v[6:7] op_sel:[0,1] op_sel_hi:[1,0] neg_lo:[0,1]
	v_pk_add_f32 v[24:25], v[24:25], v[36:37] neg_lo:[0,1] neg_hi:[0,1]
	v_pk_add_f32 v[34:35], v[22:23], v[32:33]
	v_pk_add_f32 v[32:33], v[22:23], v[32:33] neg_lo:[0,1] neg_hi:[0,1]
	v_pk_mul_f32 v[54:55], v[2:3], s[12:13]
	v_pk_add_f32 v[36:37], v[8:9], v[24:25] op_sel:[0,1] op_sel_hi:[1,0] neg_hi:[0,1]
	v_pk_add_f32 v[8:9], v[8:9], v[24:25] op_sel:[0,1] op_sel_hi:[1,0] neg_lo:[0,1]
	v_pk_mul_f32 v[22:23], v[4:5], s[10:11] op_sel:[0,0] op_sel_hi:[0,1]
	v_pk_fma_f32 v[22:23], v[4:5], s[10:11], v[22:23] op_sel:[1,1,0] op_sel_hi:[1,0,1] neg_lo:[0,1,0]
	v_pk_add_f32 v[4:5], v[28:29], v[34:35]
	v_pk_add_f32 v[2:3], v[32:33], v[32:33] op_sel:[0,1] op_sel_hi:[1,0] neg_lo:[0,1]
	v_pk_add_f32 v[28:29], v[28:29], v[34:35] neg_lo:[0,1] neg_hi:[0,1]
	v_pk_mul_f32 v[32:33], v[2:3], s[12:13]
	v_pk_add_f32 v[2:3], v[26:27], v[30:31]
	v_pk_add_f32 v[26:27], v[26:27], v[30:31] neg_lo:[0,1] neg_hi:[0,1]
	v_pk_mul_f32 v[24:25], v[10:11], s[6:7] op_sel:[0,0] op_sel_hi:[0,1]
	v_pk_fma_f32 v[24:25], v[10:11], s[6:7], v[24:25] op_sel:[1,1,0] op_sel_hi:[1,0,1] neg_lo:[0,1,0]
	v_pk_mul_f32 v[6:7], v[36:37], s[10:11] op_sel:[0,0] op_sel_hi:[0,1]
	v_pk_fma_f32 v[6:7], v[36:37], s[10:11], v[6:7] op_sel:[1,1,0] op_sel_hi:[1,0,1] neg_lo:[0,1,0]
	v_pk_mul_f32 v[56:57], v[8:9], s[14:15] op_sel:[0,0] op_sel_hi:[0,1]
	v_pk_fma_f32 v[56:57], v[8:9], s[14:15], v[56:57] op_sel:[1,1,0] op_sel_hi:[1,0,1] neg_lo:[0,1,0]
	v_pk_add_f32 v[10:11], v[2:3], v[4:5]
	v_lshlrev_b32_e32 v34, 2, v0
	v_pk_add_f32 v[4:5], v[2:3], v[4:5] neg_lo:[0,1] neg_hi:[0,1]
	v_pk_add_f32 v[8:9], v[26:27], v[28:29] op_sel:[0,1] op_sel_hi:[1,0] neg_hi:[0,1]
	v_pk_add_f32 v[2:3], v[26:27], v[28:29] op_sel:[0,1] op_sel_hi:[1,0] neg_lo:[0,1]
	v_pk_add_f32 v[26:27], v[14:15], v[12:13]
	v_pk_add_f32 v[28:29], v[24:25], v[6:7]
	v_add_u32_e32 v1, 0x400, v34
	v_pk_add_f32 v[14:15], v[14:15], v[12:13] neg_lo:[0,1] neg_hi:[0,1]
	v_pk_add_f32 v[30:31], v[24:25], v[6:7] neg_lo:[0,1] neg_hi:[0,1]
	v_pk_add_f32 v[12:13], v[26:27], v[28:29]
	v_pk_add_f32 v[6:7], v[26:27], v[28:29] neg_lo:[0,1] neg_hi:[0,1]
	v_add_u32_e32 v24, 0x800, v34
	v_add_u32_e32 v25, 0xc00, v34
	v_add_u32_e32 v26, 0x1000, v34
	v_add_u32_e32 v27, 0x1400, v34
	v_add_u32_e32 v28, 0x1800, v34
	v_add_u32_e32 v29, 0x1c00, v34
	v_add_u32_e32 v35, 0x2000, v34
	s_waitcnt vmcnt(0)
	v_mov_b32_e32 v1, v113
	s_nop 0
	v_mov_b32_e32 v36, v114
	v_mov_b32_e32 v37, v115
	v_mov_b32_e32 v38, v116
	v_mov_b32_e32 v39, v117
	v_mov_b32_e32 v40, v118
	v_mov_b32_e32 v41, v119
	v_mov_b32_e32 v42, v120
	v_add_u32_e32 v24, 0x2400, v34
	v_add_u32_e32 v25, 0x2800, v34
	v_add_u32_e32 v26, 0x2c00, v34
	v_add_u32_e32 v27, 0x3000, v34
	v_add_u32_e32 v28, 0x3400, v34
	v_add_u32_e32 v35, 0x3800, v34
	v_mov_b32_e32 v52, v112
	v_mov_b32_e32 v43, v126
	v_add_u32_e32 v29, 0x3c00, v34
	v_mov_b32_e32 v47, v121
	v_mov_b32_e32 v48, v122
	v_mov_b32_e32 v49, v123
	v_mov_b32_e32 v50, v124
	v_mov_b32_e32 v51, v125
	v_mov_b32_e32 v46, v127
	v_pk_add_f32 v[26:27], v[16:17], v[20:21] op_sel:[0,1] op_sel_hi:[1,0] neg_hi:[0,1]
	v_pk_add_f32 v[16:17], v[16:17], v[20:21] op_sel:[0,1] op_sel_hi:[1,0] neg_lo:[0,1]
	v_pk_add_f32 v[20:21], v[44:45], v[32:33]
	v_pk_add_f32 v[28:29], v[44:45], v[32:33] neg_lo:[0,1] neg_hi:[0,1]
	v_pk_add_f32 v[24:25], v[14:15], v[30:31] op_sel:[0,1] op_sel_hi:[1,0] neg_hi:[0,1]
	v_pk_add_f32 v[14:15], v[14:15], v[30:31] op_sel:[0,1] op_sel_hi:[1,0] neg_lo:[0,1]
	v_pk_add_f32 v[30:31], v[20:21], v[26:27]
	v_pk_add_f32 v[20:21], v[26:27], v[20:21] neg_lo:[0,1] neg_hi:[0,1]
	v_pk_add_f32 v[26:27], v[16:17], v[28:29] op_sel:[0,1] op_sel_hi:[1,0] neg_hi:[0,1]
	v_pk_add_f32 v[16:17], v[16:17], v[28:29] op_sel:[0,1] op_sel_hi:[1,0] neg_lo:[0,1]
	v_pk_add_f32 v[28:29], v[18:19], v[54:55]
	v_pk_add_f32 v[44:45], v[22:23], v[56:57]
	s_mov_b32 s2, 0xff61b1e6
	v_pk_add_f32 v[18:19], v[18:19], v[54:55] neg_lo:[0,1] neg_hi:[0,1]
	v_pk_add_f32 v[54:55], v[22:23], v[56:57] neg_lo:[0,1] neg_hi:[0,1]
	v_pk_add_f32 v[32:33], v[28:29], v[44:45]
	v_pk_add_f32 v[22:23], v[28:29], v[44:45] neg_lo:[0,1] neg_hi:[0,1]
	v_max3_f32 v44, v10, s2, v12
	v_max3_f32 v44, v44, v30, v32
	v_max3_f32 v44, v44, v8, v24
	v_pk_add_f32 v[28:29], v[18:19], v[54:55] op_sel:[0,1] op_sel_hi:[1,0] neg_hi:[0,1]
	v_pk_add_f32 v[18:19], v[18:19], v[54:55] op_sel:[0,1] op_sel_hi:[1,0] neg_lo:[0,1]
	v_max3_f32 v45, -v11, s2, -v13
	v_max3_f32 v44, v44, v26, v28
	v_max3_f32 v44, v44, v4, v6
	v_max3_f32 v44, v44, v20, v22
	v_max3_f32 v44, v44, v2, v14
	v_max3_f32 v44, v44, v16, v18
	v_max3_f32 v45, v45, -v31, -v33
	v_max3_f32 v45, v45, -v9, -v25
	v_mov_b32_dpp v53, v44 quad_perm:[1,0,3,2] row_mask:0xf bank_mask:0xf
	v_max_f32_e32 v53, v53, v53
	v_max_f32_e32 v44, v44, v53
	v_mov_b32_e32 v53, 0
	v_max3_f32 v45, v45, -v27, -v29
	v_max3_f32 v45, v45, -v5, -v7
	v_mov_b32_dpp v53, v44 quad_perm:[2,3,0,1] row_mask:0xf bank_mask:0xf
	v_max_f32_e32 v53, v53, v53
	v_max_f32_e32 v44, v44, v53
	v_mov_b32_e32 v53, 0
	v_max3_f32 v45, v45, -v21, -v23
	v_max3_f32 v45, v45, -v3, -v15
	v_mov_b32_dpp v53, v44 row_half_mirror row_mask:0xf bank_mask:0xf
	v_max_f32_e32 v53, v53, v53
	v_max_f32_e32 v44, v44, v53
	v_mov_b32_e32 v53, 0
	v_max3_f32 v45, v45, -v17, -v19
	s_nop 0
	v_mov_b32_dpp v53, v44 row_mirror row_mask:0xf bank_mask:0xf
	v_max_f32_e32 v53, v53, v53
	v_max_f32_e32 v44, v44, v53
	s_nop 0
	v_readlane_b32 s5, v44, 0
	v_readlane_b32 s6, v44, 16
	v_readlane_b32 s7, v44, 32
	v_readlane_b32 s8, v44, 48
	v_mov_b32_e32 v44, 0
	s_nop 1
	v_mov_b32_dpp v44, v45 quad_perm:[1,0,3,2] row_mask:0xf bank_mask:0xf
	v_max_f32_e32 v44, v44, v44
	v_max_f32_e32 v44, v45, v44
	v_mov_b32_e32 v45, 0
	s_nop 1
	v_mov_b32_dpp v45, v44 quad_perm:[2,3,0,1] row_mask:0xf bank_mask:0xf
	v_max_f32_e32 v45, v45, v45
	v_max_f32_e32 v44, v44, v45
	v_mov_b32_e32 v45, 0
	s_nop 1
	v_mov_b32_dpp v45, v44 row_half_mirror row_mask:0xf bank_mask:0xf
	v_max_f32_e32 v45, v45, v45
	v_max_f32_e32 v44, v44, v45
	v_mov_b32_e32 v45, 0
	s_nop 1
	v_mov_b32_dpp v45, v44 row_mirror row_mask:0xf bank_mask:0xf
	v_max_f32_e32 v45, v45, v45
	v_max_f32_e32 v44, v44, v45
	v_and_b32_e32 v45, 63, v0
	v_readlane_b32 s9, v44, 0
	v_readlane_b32 s10, v44, 16
	v_readlane_b32 s11, v44, 32
	v_readlane_b32 s12, v44, 48
	v_ashrrev_i32_e32 v44, 6, v0
	v_cmp_eq_u32_e32 vcc, 0, v45
	v_lshlrev_b32_e32 v61, 3, v44
	s_and_saveexec_b64 s[2:3], vcc
	s_cbranch_execz .LBB1_10
	v_max_f32_e64 v44, s12, s12
	v_max_f32_e64 v45, s11, s11
	v_max_f32_e32 v44, v45, v44
	v_mov_b32_e32 v45, s10
	v_max3_f32 v45, s9, v45, v44
	v_max_f32_e64 v44, s8, s8
	v_max_f32_e64 v53, s7, s7
	v_max_f32_e32 v44, v53, v44
	v_mov_b32_e32 v53, s6
	v_max3_f32 v44, s5, v53, v44
	ds_write_b64 v61, v[44:45] offset:36864
